# v13 + load segments at s_setprio 2 + 64-byte K-loop alignment
# speedup vs baseline: 1.0079x; 1.0079x over previous
.LBB0_286:
	s_lshl_b32 s10, s51, 19
	s_add_u32 s10, s20, s10
	s_addc_u32 s11, s21, 0
	s_and_b64 s[16:17], s[4:5], exec
	s_cselect_b32 s54, s11, s31
	s_cselect_b32 s55, s10, s30
	s_lshl_b32 s14, s50, 19
	s_add_u32 s16, s15, s14
	s_addc_u32 s17, s26, 0
	s_and_b64 s[36:37], s[4:5], exec
	s_cselect_b32 s56, s17, s23
	s_cselect_b32 s57, s16, s22
	s_add_i32 s60, 0, 0x10000
	v_add_u32_e32 v198, s60, v196
	s_add_i32 s62, 0, 0x14000
	v_add_u32_e32 v199, s62, v196
	ds_read_b128 v[160:163], v198
	ds_read_b128 v[152:155], v198 offset:1024
	ds_read_b128 v[156:159], v198 offset:2048
	ds_read_b128 v[148:151], v198 offset:3072
	ds_read_b128 v[144:147], v199
	ds_read_b128 v[136:139], v199 offset:1024
	ds_read_b128 v[140:143], v199 offset:2048
	ds_read_b128 v[132:135], v199 offset:3072
	s_add_u32 s36, s30, 0x40080
	s_addc_u32 s37, s31, 0
	s_add_i32 s58, s41, 0xc000
	v_lshl_add_u64 v[174:175], s[36:37], 0, v[168:169]
	s_mov_b32 m0, s58
	s_add_i32 s59, s41, 0xe000
	ds_read_b128 v[178:181], v197
	ds_read_b128 v[182:185], v197 offset:1024
	ds_read_b128 v[190:193], v197 offset:2048
	ds_read_b128 v[200:203], v197 offset:3072
	ds_read_b128 v[204:207], v197 offset:4096
	ds_read_b128 v[208:211], v197 offset:5120
	ds_read_b128 v[212:215], v197 offset:6144
	ds_read_b128 v[216:219], v197 offset:7168
	global_load_lds_dwordx4 v[174:175], off
	v_lshl_add_u64 v[174:175], s[36:37], 0, v[166:167]
	s_mov_b32 m0, s59
	s_nop 0
	global_load_lds_dwordx4 v[174:175], off
	s_waitcnt vmcnt(8)
	s_waitcnt lgkmcnt(0)
	s_barrier
	s_setprio 1
	s_waitcnt lgkmcnt(0)
	v_mfma_f32_16x16x32_bf16 v[128:131], v[160:163], v[178:181], 0
	v_mfma_f32_16x16x32_bf16 v[124:127], v[156:159], v[178:181], 0
	v_mfma_f32_16x16x32_bf16 v[116:119], v[156:159], v[190:193], 0
	v_mfma_f32_16x16x32_bf16 v[120:123], v[160:163], v[190:193], 0
	v_mfma_f32_16x16x32_bf16 v[112:115], v[160:163], v[204:207], 0
	v_mfma_f32_16x16x32_bf16 v[108:111], v[156:159], v[204:207], 0
	v_mfma_f32_16x16x32_bf16 v[100:103], v[156:159], v[212:215], 0
	v_mfma_f32_16x16x32_bf16 v[104:107], v[160:163], v[212:215], 0
	s_nop 0
	v_mfma_f32_16x16x32_bf16 v[128:131], v[152:155], v[182:185], v[128:131]
	v_mfma_f32_16x16x32_bf16 v[124:127], v[148:151], v[182:185], v[124:127]
	v_mfma_f32_16x16x32_bf16 v[116:119], v[148:151], v[200:203], v[116:119]
	v_mfma_f32_16x16x32_bf16 v[120:123], v[152:155], v[200:203], v[120:123]
	v_mfma_f32_16x16x32_bf16 v[112:115], v[152:155], v[208:211], v[112:115]
	v_mfma_f32_16x16x32_bf16 v[108:111], v[148:151], v[208:211], v[108:111]
	v_mfma_f32_16x16x32_bf16 v[100:103], v[148:151], v[216:219], v[100:103]
	v_mfma_f32_16x16x32_bf16 v[104:107], v[152:155], v[216:219], v[104:107]
	s_setprio 2
	s_setprio 1
	v_mfma_f32_16x16x32_bf16 v[96:99], v[144:147], v[178:181], 0
	v_mfma_f32_16x16x32_bf16 v[92:95], v[140:143], v[178:181], 0
	v_mfma_f32_16x16x32_bf16 v[84:87], v[140:143], v[190:193], 0
	v_mfma_f32_16x16x32_bf16 v[88:91], v[144:147], v[190:193], 0
	v_mfma_f32_16x16x32_bf16 v[80:83], v[144:147], v[204:207], 0
	v_mfma_f32_16x16x32_bf16 v[76:79], v[140:143], v[204:207], 0
	v_mfma_f32_16x16x32_bf16 v[68:71], v[140:143], v[212:215], 0
	v_mfma_f32_16x16x32_bf16 v[72:75], v[144:147], v[212:215], 0
	s_nop 0
	v_mfma_f32_16x16x32_bf16 v[96:99], v[136:139], v[182:185], v[96:99]
	v_mfma_f32_16x16x32_bf16 v[92:95], v[132:135], v[182:185], v[92:95]
	v_mfma_f32_16x16x32_bf16 v[84:87], v[132:135], v[200:203], v[84:87]
	v_mfma_f32_16x16x32_bf16 v[88:91], v[136:139], v[200:203], v[88:91]
	v_mfma_f32_16x16x32_bf16 v[80:83], v[136:139], v[208:211], v[80:83]
	v_mfma_f32_16x16x32_bf16 v[76:79], v[132:135], v[208:211], v[76:79]
	v_mfma_f32_16x16x32_bf16 v[68:71], v[132:135], v[216:219], v[68:71]
	v_mfma_f32_16x16x32_bf16 v[72:75], v[136:139], v[216:219], v[72:75]
	s_setprio 2
	s_barrier
	v_lshl_add_u64 v[174:175], s[22:23], 0, v[34:35]
	s_add_i32 s60, s60, s40
	v_lshl_add_u64 v[190:191], v[174:175], 0, s[28:29]
	s_mov_b32 m0, s60
	s_add_i32 s61, s60, 0x2000
	ds_read_b128 v[178:181], v197 offset:16384
	ds_read_b128 v[182:185], v197 offset:17408
	ds_read_b128 v[200:203], v197 offset:18432
	ds_read_b128 v[204:207], v197 offset:19456
	ds_read_b128 v[208:211], v197 offset:20480
	ds_read_b128 v[212:215], v197 offset:21504
	ds_read_b128 v[216:219], v197 offset:22528
	ds_read_b128 v[222:225], v197 offset:23552
	global_load_lds_dwordx4 v[190:191], off
	v_lshl_add_u64 v[190:191], s[22:23], 0, v[164:165]
	s_add_u32 s36, s22, 0x40100
	v_lshl_add_u64 v[192:193], v[190:191], 0, s[28:29]
	s_mov_b32 m0, s61
	s_addc_u32 s37, s23, 0
	s_add_i32 s62, s62, s40
	global_load_lds_dwordx4 v[192:193], off
	v_lshl_add_u64 v[192:193], s[36:37], 0, v[34:35]
	s_mov_b32 m0, s62
	s_add_i32 s63, s62, 0x2000
	global_load_lds_dwordx4 v[192:193], off
	v_lshl_add_u64 v[192:193], s[36:37], 0, v[164:165]
	s_mov_b32 m0, s63
	s_nop 0
	global_load_lds_dwordx4 v[192:193], off
	v_lshl_add_u64 v[192:193], s[30:31], 0, v[168:169]
	v_lshl_add_u64 v[194:195], v[192:193], 0, s[28:29]
	s_mov_b32 m0, s41
	s_nop 0
	global_load_lds_dwordx4 v[194:195], off
	v_lshl_add_u64 v[194:195], s[30:31], 0, v[166:167]
	v_lshl_add_u64 v[226:227], v[194:195], 0, s[28:29]
	s_mov_b32 m0, s42
	s_nop 0
	global_load_lds_dwordx4 v[226:227], off
	s_waitcnt vmcnt(8)
	s_waitcnt lgkmcnt(0)
	s_barrier
	s_setprio 1
	s_waitcnt lgkmcnt(0)
	v_mfma_f32_16x16x32_bf16 v[64:67], v[160:163], v[178:181], 0
	v_mfma_f32_16x16x32_bf16 v[60:63], v[156:159], v[178:181], 0
	v_mfma_f32_16x16x32_bf16 v[52:55], v[156:159], v[200:203], 0
	v_mfma_f32_16x16x32_bf16 v[56:59], v[160:163], v[200:203], 0
	v_mfma_f32_16x16x32_bf16 v[48:51], v[160:163], v[208:211], 0
	v_mfma_f32_16x16x32_bf16 v[44:47], v[156:159], v[208:211], 0
	v_mfma_f32_16x16x32_bf16 v[36:39], v[156:159], v[216:219], 0
	v_mfma_f32_16x16x32_bf16 v[40:43], v[160:163], v[216:219], 0
	s_nop 0
	v_mfma_f32_16x16x32_bf16 v[64:67], v[152:155], v[182:185], v[64:67]
	v_mfma_f32_16x16x32_bf16 v[60:63], v[148:151], v[182:185], v[60:63]
	v_mfma_f32_16x16x32_bf16 v[52:55], v[148:151], v[204:207], v[52:55]
	v_mfma_f32_16x16x32_bf16 v[56:59], v[152:155], v[204:207], v[56:59]
	v_mfma_f32_16x16x32_bf16 v[48:51], v[152:155], v[212:215], v[48:51]
	v_mfma_f32_16x16x32_bf16 v[44:47], v[148:151], v[212:215], v[44:47]
	v_mfma_f32_16x16x32_bf16 v[36:39], v[148:151], v[222:225], v[36:39]
	v_mfma_f32_16x16x32_bf16 v[40:43], v[152:155], v[222:225], v[40:43]
	s_setprio 2
	s_setprio 1
	v_mfma_f32_16x16x32_bf16 v[30:33], v[144:147], v[178:181], 0
	v_mfma_f32_16x16x32_bf16 v[26:29], v[140:143], v[178:181], 0
	v_mfma_f32_16x16x32_bf16 v[18:21], v[140:143], v[200:203], 0
	v_mfma_f32_16x16x32_bf16 v[22:25], v[144:147], v[200:203], 0
	v_mfma_f32_16x16x32_bf16 v[14:17], v[144:147], v[208:211], 0
	v_mfma_f32_16x16x32_bf16 v[10:13], v[140:143], v[208:211], 0
	v_mfma_f32_16x16x32_bf16 v[2:5], v[140:143], v[216:219], 0
	v_mfma_f32_16x16x32_bf16 v[6:9], v[144:147], v[216:219], 0
	s_nop 0
	v_mfma_f32_16x16x32_bf16 v[30:33], v[136:139], v[182:185], v[30:33]
	v_mfma_f32_16x16x32_bf16 v[26:29], v[132:135], v[182:185], v[26:29]
	v_mfma_f32_16x16x32_bf16 v[18:21], v[132:135], v[204:207], v[18:21]
	v_mfma_f32_16x16x32_bf16 v[22:25], v[136:139], v[204:207], v[22:25]
	v_mfma_f32_16x16x32_bf16 v[14:17], v[136:139], v[212:215], v[14:17]
	v_mfma_f32_16x16x32_bf16 v[10:13], v[132:135], v[212:215], v[10:13]
	v_mfma_f32_16x16x32_bf16 v[2:5], v[132:135], v[222:225], v[2:5]
	v_mfma_f32_16x16x32_bf16 v[6:9], v[136:139], v[222:225], v[6:9]
	s_setprio 2
	s_barrier
	s_add_i32 s64, 0, 0x18000
	s_add_i32 s66, 0, 0x1c000
	v_add_u32_e32 v132, s64, v196
	v_add_u32_e32 v133, s66, v196
	ds_read_b128 v[134:137], v132
	ds_read_b128 v[138:141], v132 offset:1024
	ds_read_b128 v[142:145], v132 offset:2048
	ds_read_b128 v[146:149], v132 offset:3072
	ds_read_b128 v[150:153], v133
	ds_read_b128 v[154:157], v133 offset:1024
	ds_read_b128 v[158:161], v133 offset:2048
	ds_read_b128 v[178:181], v133 offset:3072
	s_add_u32 s36, s30, 0x40100
	s_addc_u32 s37, s31, 0
	s_mov_b32 m0, s43
	v_lshl_add_u64 v[162:163], s[36:37], 0, v[168:169]
	ds_read_b128 v[182:185], v197 offset:32768
	ds_read_b128 v[200:203], v197 offset:33792
	ds_read_b128 v[204:207], v197 offset:34816
	ds_read_b128 v[208:211], v197 offset:35840
	ds_read_b128 v[212:215], v197 offset:36864
	ds_read_b128 v[216:219], v197 offset:37888
	ds_read_b128 v[222:225], v197 offset:38912
	ds_read_b128 v[226:229], v197 offset:39936
	global_load_lds_dwordx4 v[162:163], off
	v_lshl_add_u64 v[162:163], s[36:37], 0, v[166:167]
	s_mov_b32 m0, s44
	s_nop 0
	global_load_lds_dwordx4 v[162:163], off
	s_waitcnt vmcnt(8)
	s_waitcnt lgkmcnt(0)
	s_barrier
	s_setprio 1
	s_waitcnt lgkmcnt(0)
	v_mfma_f32_16x16x32_bf16 v[128:131], v[134:137], v[182:185], v[128:131]
	v_mfma_f32_16x16x32_bf16 v[124:127], v[142:145], v[182:185], v[124:127]
	v_mfma_f32_16x16x32_bf16 v[116:119], v[142:145], v[204:207], v[116:119]
	v_mfma_f32_16x16x32_bf16 v[120:123], v[134:137], v[204:207], v[120:123]
	v_mfma_f32_16x16x32_bf16 v[112:115], v[134:137], v[212:215], v[112:115]
	v_mfma_f32_16x16x32_bf16 v[108:111], v[142:145], v[212:215], v[108:111]
	v_mfma_f32_16x16x32_bf16 v[100:103], v[142:145], v[222:225], v[100:103]
	v_mfma_f32_16x16x32_bf16 v[104:107], v[134:137], v[222:225], v[104:107]
	v_mfma_f32_16x16x32_bf16 v[128:131], v[138:141], v[200:203], v[128:131]
	v_mfma_f32_16x16x32_bf16 v[124:127], v[146:149], v[200:203], v[124:127]
	v_mfma_f32_16x16x32_bf16 v[116:119], v[146:149], v[208:211], v[116:119]
	v_mfma_f32_16x16x32_bf16 v[120:123], v[138:141], v[208:211], v[120:123]
	v_mfma_f32_16x16x32_bf16 v[112:115], v[138:141], v[216:219], v[112:115]
	v_mfma_f32_16x16x32_bf16 v[108:111], v[146:149], v[216:219], v[108:111]
	v_mfma_f32_16x16x32_bf16 v[100:103], v[146:149], v[226:229], v[100:103]
	v_mfma_f32_16x16x32_bf16 v[104:107], v[138:141], v[226:229], v[104:107]
	s_setprio 2
	s_setprio 1
	v_mfma_f32_16x16x32_bf16 v[96:99], v[150:153], v[182:185], v[96:99]
	v_mfma_f32_16x16x32_bf16 v[92:95], v[158:161], v[182:185], v[92:95]
	v_mfma_f32_16x16x32_bf16 v[84:87], v[158:161], v[204:207], v[84:87]
	v_mfma_f32_16x16x32_bf16 v[88:91], v[150:153], v[204:207], v[88:91]
	v_mfma_f32_16x16x32_bf16 v[80:83], v[150:153], v[212:215], v[80:83]
	v_mfma_f32_16x16x32_bf16 v[76:79], v[158:161], v[212:215], v[76:79]
	v_mfma_f32_16x16x32_bf16 v[68:71], v[158:161], v[222:225], v[68:71]
	v_mfma_f32_16x16x32_bf16 v[72:75], v[150:153], v[222:225], v[72:75]
	v_mfma_f32_16x16x32_bf16 v[96:99], v[154:157], v[200:203], v[96:99]
	v_mfma_f32_16x16x32_bf16 v[92:95], v[178:181], v[200:203], v[92:95]
	v_mfma_f32_16x16x32_bf16 v[84:87], v[178:181], v[208:211], v[84:87]
	v_mfma_f32_16x16x32_bf16 v[88:91], v[154:157], v[208:211], v[88:91]
	v_mfma_f32_16x16x32_bf16 v[80:83], v[154:157], v[216:219], v[80:83]
	v_mfma_f32_16x16x32_bf16 v[76:79], v[178:181], v[216:219], v[76:79]
	v_mfma_f32_16x16x32_bf16 v[68:71], v[178:181], v[226:229], v[68:71]
	v_mfma_f32_16x16x32_bf16 v[72:75], v[154:157], v[226:229], v[72:75]
	s_setprio 2
	s_barrier
	s_add_i32 s64, s64, s40
	s_mov_b64 s[24:25], 0x180
	s_add_i32 s65, s64, 0x2000
	v_lshl_add_u64 v[162:163], v[174:175], 0, s[24:25]
	s_mov_b32 m0, s64
	s_add_u32 s36, s22, 0x40180
	ds_read_b128 v[182:185], v197 offset:49152
	ds_read_b128 v[200:203], v197 offset:50176
	ds_read_b128 v[204:207], v197 offset:51200
	ds_read_b128 v[208:211], v197 offset:52224
	ds_read_b128 v[212:215], v197 offset:53248
	ds_read_b128 v[216:219], v197 offset:54272
	ds_read_b128 v[222:225], v197 offset:55296
	ds_read_b128 v[226:229], v197 offset:56320
	global_load_lds_dwordx4 v[162:163], off
	v_lshl_add_u64 v[162:163], v[190:191], 0, s[24:25]
	s_mov_b32 m0, s65
	s_addc_u32 s37, s23, 0
	s_add_i32 s66, s66, s40
	global_load_lds_dwordx4 v[162:163], off
	v_lshl_add_u64 v[162:163], s[36:37], 0, v[34:35]
	s_mov_b32 m0, s66
	s_add_i32 s67, s66, 0x2000
	global_load_lds_dwordx4 v[162:163], off
	v_lshl_add_u64 v[162:163], s[36:37], 0, v[164:165]
	s_mov_b32 m0, s67
	s_nop 0
	global_load_lds_dwordx4 v[162:163], off
	v_lshl_add_u64 v[162:163], v[192:193], 0, s[24:25]
	s_mov_b32 m0, s47
	s_nop 0
	global_load_lds_dwordx4 v[162:163], off
	v_lshl_add_u64 v[162:163], v[194:195], 0, s[24:25]
	s_mov_b32 m0, s48
	s_nop 0
	global_load_lds_dwordx4 v[162:163], off
	s_waitcnt vmcnt(8)
	s_waitcnt lgkmcnt(0)
	s_barrier
	s_setprio 1
	s_waitcnt lgkmcnt(0)
	v_mfma_f32_16x16x32_bf16 v[64:67], v[134:137], v[182:185], v[64:67]
	v_mfma_f32_16x16x32_bf16 v[60:63], v[142:145], v[182:185], v[60:63]
	v_mfma_f32_16x16x32_bf16 v[52:55], v[142:145], v[204:207], v[52:55]
	v_mfma_f32_16x16x32_bf16 v[56:59], v[134:137], v[204:207], v[56:59]
	v_mfma_f32_16x16x32_bf16 v[48:51], v[134:137], v[212:215], v[48:51]
	v_mfma_f32_16x16x32_bf16 v[44:47], v[142:145], v[212:215], v[44:47]
	v_mfma_f32_16x16x32_bf16 v[36:39], v[142:145], v[222:225], v[36:39]
	v_mfma_f32_16x16x32_bf16 v[40:43], v[134:137], v[222:225], v[40:43]
	v_mfma_f32_16x16x32_bf16 v[64:67], v[138:141], v[200:203], v[64:67]
	v_mfma_f32_16x16x32_bf16 v[60:63], v[146:149], v[200:203], v[60:63]
	v_mfma_f32_16x16x32_bf16 v[52:55], v[146:149], v[208:211], v[52:55]
	v_mfma_f32_16x16x32_bf16 v[56:59], v[138:141], v[208:211], v[56:59]
	v_mfma_f32_16x16x32_bf16 v[48:51], v[138:141], v[216:219], v[48:51]
	v_mfma_f32_16x16x32_bf16 v[44:47], v[146:149], v[216:219], v[44:47]
	v_mfma_f32_16x16x32_bf16 v[36:39], v[146:149], v[226:229], v[36:39]
	v_mfma_f32_16x16x32_bf16 v[40:43], v[138:141], v[226:229], v[40:43]
	s_setprio 2
	s_setprio 1
	v_mfma_f32_16x16x32_bf16 v[30:33], v[150:153], v[182:185], v[30:33]
	v_mfma_f32_16x16x32_bf16 v[26:29], v[158:161], v[182:185], v[26:29]
	v_mfma_f32_16x16x32_bf16 v[18:21], v[158:161], v[204:207], v[18:21]
	v_mfma_f32_16x16x32_bf16 v[22:25], v[150:153], v[204:207], v[22:25]
	v_mfma_f32_16x16x32_bf16 v[14:17], v[150:153], v[212:215], v[14:17]
	v_mfma_f32_16x16x32_bf16 v[10:13], v[158:161], v[212:215], v[10:13]
	v_mfma_f32_16x16x32_bf16 v[2:5], v[158:161], v[222:225], v[2:5]
	v_mfma_f32_16x16x32_bf16 v[6:9], v[150:153], v[222:225], v[6:9]
	v_mfma_f32_16x16x32_bf16 v[30:33], v[154:157], v[200:203], v[30:33]
	v_mfma_f32_16x16x32_bf16 v[26:29], v[178:181], v[200:203], v[26:29]
	v_mfma_f32_16x16x32_bf16 v[18:21], v[178:181], v[208:211], v[18:21]
	v_mfma_f32_16x16x32_bf16 v[22:25], v[154:157], v[208:211], v[22:25]
	v_mfma_f32_16x16x32_bf16 v[14:17], v[154:157], v[216:219], v[14:17]
	v_mfma_f32_16x16x32_bf16 v[10:13], v[178:181], v[216:219], v[10:13]
	v_mfma_f32_16x16x32_bf16 v[2:5], v[178:181], v[226:229], v[2:5]
	v_mfma_f32_16x16x32_bf16 v[6:9], v[154:157], v[226:229], v[6:9]
	s_setprio 2
	s_barrier
	s_add_u32 s30, s30, 0x40180
	s_addc_u32 s31, s31, 0
	s_add_u32 s68, s22, 0x200
	s_addc_u32 s69, s23, 0
	s_mov_b32 s70, 0
	.p2align	6

.LBB0_540:
	s_lshl_b32 s14, s55, 19
	v_readlane_b32 s16, v253, 53
	v_readlane_b32 s17, v253, 54
	s_add_u32 s16, s16, s14
	s_addc_u32 s17, s17, 0
	s_and_b64 s[22:23], s[4:5], exec
	s_cselect_b32 s58, s17, s37
	s_cselect_b32 s59, s16, s36
	s_lshl_b32 s14, s54, 19
	s_add_u32 s22, s15, s14
	s_addc_u32 s23, s26, 0
	s_and_b64 s[40:41], s[4:5], exec
	s_cselect_b32 s60, s23, s31
	s_cselect_b32 s61, s22, s30
	s_add_i32 s64, 0, 0x10000
	v_add_u32_e32 v172, s64, v222
	s_add_i32 s66, 0, 0x14000
	v_add_u32_e32 v173, s66, v222
	ds_read_b128 v[160:163], v172
	ds_read_b128 v[152:155], v172 offset:1024
	ds_read_b128 v[156:159], v172 offset:2048
	ds_read_b128 v[148:151], v172 offset:3072
	ds_read_b128 v[144:147], v173
	ds_read_b128 v[136:139], v173 offset:1024
	ds_read_b128 v[140:143], v173 offset:2048
	ds_read_b128 v[132:135], v173 offset:3072
	s_add_u32 s40, s36, 0x40080
	s_addc_u32 s41, s37, 0
	s_add_i32 s62, s43, 0xc000
	v_lshl_add_u64 v[174:175], s[40:41], 0, v[194:195]
	s_mov_b32 m0, s62
	s_add_i32 s63, s43, 0xe000
	ds_read_b128 v[164:167], v223
	ds_read_b128 v[168:171], v223 offset:1024
	ds_read_b128 v[178:181], v223 offset:2048
	ds_read_b128 v[182:185], v223 offset:3072
	ds_read_b128 v[200:203], v223 offset:4096
	ds_read_b128 v[204:207], v223 offset:5120
	ds_read_b128 v[208:211], v223 offset:6144
	ds_read_b128 v[212:215], v223 offset:7168
	global_load_lds_dwordx4 v[174:175], off
	v_lshl_add_u64 v[174:175], s[40:41], 0, v[192:193]
	s_mov_b32 m0, s63
	s_nop 0
	global_load_lds_dwordx4 v[174:175], off
	s_waitcnt vmcnt(8)
	s_waitcnt lgkmcnt(0)
	s_barrier
	s_setprio 1
	s_waitcnt lgkmcnt(0)
	v_mfma_f32_16x16x32_bf16 v[128:131], v[160:163], v[164:167], 0
	v_mfma_f32_16x16x32_bf16 v[124:127], v[156:159], v[164:167], 0
	v_mfma_f32_16x16x32_bf16 v[116:119], v[156:159], v[178:181], 0
	v_mfma_f32_16x16x32_bf16 v[120:123], v[160:163], v[178:181], 0
	v_mfma_f32_16x16x32_bf16 v[112:115], v[160:163], v[200:203], 0
	v_mfma_f32_16x16x32_bf16 v[108:111], v[156:159], v[200:203], 0
	v_mfma_f32_16x16x32_bf16 v[100:103], v[156:159], v[208:211], 0
	v_mfma_f32_16x16x32_bf16 v[104:107], v[160:163], v[208:211], 0
	s_nop 0
	v_mfma_f32_16x16x32_bf16 v[128:131], v[152:155], v[168:171], v[128:131]
	v_mfma_f32_16x16x32_bf16 v[124:127], v[148:151], v[168:171], v[124:127]
	v_mfma_f32_16x16x32_bf16 v[116:119], v[148:151], v[182:185], v[116:119]
	v_mfma_f32_16x16x32_bf16 v[120:123], v[152:155], v[182:185], v[120:123]
	v_mfma_f32_16x16x32_bf16 v[112:115], v[152:155], v[204:207], v[112:115]
	v_mfma_f32_16x16x32_bf16 v[108:111], v[148:151], v[204:207], v[108:111]
	v_mfma_f32_16x16x32_bf16 v[100:103], v[148:151], v[212:215], v[100:103]
	v_mfma_f32_16x16x32_bf16 v[104:107], v[152:155], v[212:215], v[104:107]
	s_setprio 2
	s_setprio 1
	v_mfma_f32_16x16x32_bf16 v[96:99], v[144:147], v[164:167], 0
	v_mfma_f32_16x16x32_bf16 v[92:95], v[140:143], v[164:167], 0
	v_mfma_f32_16x16x32_bf16 v[84:87], v[140:143], v[178:181], 0
	v_mfma_f32_16x16x32_bf16 v[88:91], v[144:147], v[178:181], 0
	v_mfma_f32_16x16x32_bf16 v[80:83], v[144:147], v[200:203], 0
	v_mfma_f32_16x16x32_bf16 v[76:79], v[140:143], v[200:203], 0
	v_mfma_f32_16x16x32_bf16 v[68:71], v[140:143], v[208:211], 0
	v_mfma_f32_16x16x32_bf16 v[72:75], v[144:147], v[208:211], 0
	s_nop 0
	v_mfma_f32_16x16x32_bf16 v[96:99], v[136:139], v[168:171], v[96:99]
	v_mfma_f32_16x16x32_bf16 v[92:95], v[132:135], v[168:171], v[92:95]
	v_mfma_f32_16x16x32_bf16 v[84:87], v[132:135], v[182:185], v[84:87]
	v_mfma_f32_16x16x32_bf16 v[88:91], v[136:139], v[182:185], v[88:91]
	v_mfma_f32_16x16x32_bf16 v[80:83], v[136:139], v[204:207], v[80:83]
	v_mfma_f32_16x16x32_bf16 v[76:79], v[132:135], v[204:207], v[76:79]
	v_mfma_f32_16x16x32_bf16 v[68:71], v[132:135], v[212:215], v[68:71]
	v_mfma_f32_16x16x32_bf16 v[72:75], v[136:139], v[212:215], v[72:75]
	s_setprio 2
	s_barrier
	v_lshl_add_u64 v[164:165], s[30:31], 0, v[34:35]
	s_add_i32 s64, s64, s42
	v_lshl_add_u64 v[166:167], v[164:165], 0, s[28:29]
	s_mov_b32 m0, s64
	s_add_i32 s65, s64, 0x2000
	ds_read_b128 v[178:181], v223 offset:16384
	ds_read_b128 v[182:185], v223 offset:17408
	ds_read_b128 v[200:203], v223 offset:18432
	ds_read_b128 v[204:207], v223 offset:19456
	ds_read_b128 v[208:211], v223 offset:20480
	ds_read_b128 v[212:215], v223 offset:21504
	ds_read_b128 v[216:219], v223 offset:22528
	ds_read_b128 v[224:227], v223 offset:23552
	global_load_lds_dwordx4 v[166:167], off
	v_lshl_add_u64 v[166:167], s[30:31], 0, v[190:191]
	s_add_u32 s40, s30, 0x40100
	v_lshl_add_u64 v[168:169], v[166:167], 0, s[28:29]
	s_mov_b32 m0, s65
	s_addc_u32 s41, s31, 0
	s_add_i32 s66, s66, s42
	global_load_lds_dwordx4 v[168:169], off
	v_lshl_add_u64 v[168:169], s[40:41], 0, v[34:35]
	s_mov_b32 m0, s66
	s_add_i32 s67, s66, 0x2000
	global_load_lds_dwordx4 v[168:169], off
	v_lshl_add_u64 v[168:169], s[40:41], 0, v[190:191]
	s_mov_b32 m0, s67
	s_nop 0
	global_load_lds_dwordx4 v[168:169], off
	v_lshl_add_u64 v[168:169], s[36:37], 0, v[194:195]
	v_lshl_add_u64 v[170:171], v[168:169], 0, s[28:29]
	s_mov_b32 m0, s43
	s_nop 0
	global_load_lds_dwordx4 v[170:171], off
	v_lshl_add_u64 v[170:171], s[36:37], 0, v[192:193]
	v_lshl_add_u64 v[174:175], v[170:171], 0, s[28:29]
	s_mov_b32 m0, s44
	s_nop 0
	global_load_lds_dwordx4 v[174:175], off
	s_waitcnt vmcnt(8)
	s_waitcnt lgkmcnt(0)
	s_barrier
	s_setprio 1
	s_waitcnt lgkmcnt(0)
	v_mfma_f32_16x16x32_bf16 v[64:67], v[160:163], v[178:181], 0
	v_mfma_f32_16x16x32_bf16 v[60:63], v[156:159], v[178:181], 0
	v_mfma_f32_16x16x32_bf16 v[52:55], v[156:159], v[200:203], 0
	v_mfma_f32_16x16x32_bf16 v[56:59], v[160:163], v[200:203], 0
	v_mfma_f32_16x16x32_bf16 v[48:51], v[160:163], v[208:211], 0
	v_mfma_f32_16x16x32_bf16 v[44:47], v[156:159], v[208:211], 0
	v_mfma_f32_16x16x32_bf16 v[36:39], v[156:159], v[216:219], 0
	v_mfma_f32_16x16x32_bf16 v[40:43], v[160:163], v[216:219], 0
	s_nop 0
	v_mfma_f32_16x16x32_bf16 v[64:67], v[152:155], v[182:185], v[64:67]
	v_mfma_f32_16x16x32_bf16 v[60:63], v[148:151], v[182:185], v[60:63]
	v_mfma_f32_16x16x32_bf16 v[52:55], v[148:151], v[204:207], v[52:55]
	v_mfma_f32_16x16x32_bf16 v[56:59], v[152:155], v[204:207], v[56:59]
	v_mfma_f32_16x16x32_bf16 v[48:51], v[152:155], v[212:215], v[48:51]
	v_mfma_f32_16x16x32_bf16 v[44:47], v[148:151], v[212:215], v[44:47]
	v_mfma_f32_16x16x32_bf16 v[36:39], v[148:151], v[224:227], v[36:39]
	v_mfma_f32_16x16x32_bf16 v[40:43], v[152:155], v[224:227], v[40:43]
	s_setprio 2
	s_setprio 1
	v_mfma_f32_16x16x32_bf16 v[30:33], v[144:147], v[178:181], 0
	v_mfma_f32_16x16x32_bf16 v[26:29], v[140:143], v[178:181], 0
	v_mfma_f32_16x16x32_bf16 v[18:21], v[140:143], v[200:203], 0
	v_mfma_f32_16x16x32_bf16 v[22:25], v[144:147], v[200:203], 0
	v_mfma_f32_16x16x32_bf16 v[14:17], v[144:147], v[208:211], 0
	v_mfma_f32_16x16x32_bf16 v[10:13], v[140:143], v[208:211], 0
	v_mfma_f32_16x16x32_bf16 v[2:5], v[140:143], v[216:219], 0
	v_mfma_f32_16x16x32_bf16 v[6:9], v[144:147], v[216:219], 0
	s_nop 0
	v_mfma_f32_16x16x32_bf16 v[30:33], v[136:139], v[182:185], v[30:33]
	v_mfma_f32_16x16x32_bf16 v[26:29], v[132:135], v[182:185], v[26:29]
	v_mfma_f32_16x16x32_bf16 v[18:21], v[132:135], v[204:207], v[18:21]
	v_mfma_f32_16x16x32_bf16 v[22:25], v[136:139], v[204:207], v[22:25]
	v_mfma_f32_16x16x32_bf16 v[14:17], v[136:139], v[212:215], v[14:17]
	v_mfma_f32_16x16x32_bf16 v[10:13], v[132:135], v[212:215], v[10:13]
	v_mfma_f32_16x16x32_bf16 v[2:5], v[132:135], v[224:227], v[2:5]
	v_mfma_f32_16x16x32_bf16 v[6:9], v[136:139], v[224:227], v[6:9]
	s_setprio 2
	s_barrier
	s_add_i32 s68, 0, 0x18000
	s_add_i32 s70, 0, 0x1c000
	v_add_u32_e32 v132, s68, v222
	v_add_u32_e32 v133, s70, v222
	ds_read_b128 v[134:137], v132
	ds_read_b128 v[138:141], v132 offset:1024
	ds_read_b128 v[142:145], v132 offset:2048
	ds_read_b128 v[146:149], v132 offset:3072
	ds_read_b128 v[150:153], v133
	ds_read_b128 v[154:157], v133 offset:1024
	ds_read_b128 v[158:161], v133 offset:2048
	ds_read_b128 v[178:181], v133 offset:3072
	s_add_u32 s40, s36, 0x40100
	s_addc_u32 s41, s37, 0
	s_mov_b32 m0, s45
	v_lshl_add_u64 v[162:163], s[40:41], 0, v[194:195]
	ds_read_b128 v[182:185], v223 offset:32768
	ds_read_b128 v[200:203], v223 offset:33792
	ds_read_b128 v[204:207], v223 offset:34816
	ds_read_b128 v[208:211], v223 offset:35840
	ds_read_b128 v[212:215], v223 offset:36864
	ds_read_b128 v[216:219], v223 offset:37888
	ds_read_b128 v[224:227], v223 offset:38912
	ds_read_b128 v[228:231], v223 offset:39936
	global_load_lds_dwordx4 v[162:163], off
	v_lshl_add_u64 v[162:163], s[40:41], 0, v[192:193]
	s_mov_b32 m0, s46
	s_nop 0
	global_load_lds_dwordx4 v[162:163], off
	s_waitcnt vmcnt(8)
	s_waitcnt lgkmcnt(0)
	s_barrier
	s_setprio 1
	s_waitcnt lgkmcnt(0)
	v_mfma_f32_16x16x32_bf16 v[128:131], v[134:137], v[182:185], v[128:131]
	v_mfma_f32_16x16x32_bf16 v[124:127], v[142:145], v[182:185], v[124:127]
	v_mfma_f32_16x16x32_bf16 v[116:119], v[142:145], v[204:207], v[116:119]
	v_mfma_f32_16x16x32_bf16 v[120:123], v[134:137], v[204:207], v[120:123]
	v_mfma_f32_16x16x32_bf16 v[112:115], v[134:137], v[212:215], v[112:115]
	v_mfma_f32_16x16x32_bf16 v[108:111], v[142:145], v[212:215], v[108:111]
	v_mfma_f32_16x16x32_bf16 v[100:103], v[142:145], v[224:227], v[100:103]
	v_mfma_f32_16x16x32_bf16 v[104:107], v[134:137], v[224:227], v[104:107]
	v_mfma_f32_16x16x32_bf16 v[128:131], v[138:141], v[200:203], v[128:131]
	v_mfma_f32_16x16x32_bf16 v[124:127], v[146:149], v[200:203], v[124:127]
	v_mfma_f32_16x16x32_bf16 v[116:119], v[146:149], v[208:211], v[116:119]
	v_mfma_f32_16x16x32_bf16 v[120:123], v[138:141], v[208:211], v[120:123]
	v_mfma_f32_16x16x32_bf16 v[112:115], v[138:141], v[216:219], v[112:115]
	v_mfma_f32_16x16x32_bf16 v[108:111], v[146:149], v[216:219], v[108:111]
	v_mfma_f32_16x16x32_bf16 v[100:103], v[146:149], v[228:231], v[100:103]
	v_mfma_f32_16x16x32_bf16 v[104:107], v[138:141], v[228:231], v[104:107]
	s_setprio 2
	s_setprio 1
	v_mfma_f32_16x16x32_bf16 v[96:99], v[150:153], v[182:185], v[96:99]
	v_mfma_f32_16x16x32_bf16 v[92:95], v[158:161], v[182:185], v[92:95]
	v_mfma_f32_16x16x32_bf16 v[84:87], v[158:161], v[204:207], v[84:87]
	v_mfma_f32_16x16x32_bf16 v[88:91], v[150:153], v[204:207], v[88:91]
	v_mfma_f32_16x16x32_bf16 v[80:83], v[150:153], v[212:215], v[80:83]
	v_mfma_f32_16x16x32_bf16 v[76:79], v[158:161], v[212:215], v[76:79]
	v_mfma_f32_16x16x32_bf16 v[68:71], v[158:161], v[224:227], v[68:71]
	v_mfma_f32_16x16x32_bf16 v[72:75], v[150:153], v[224:227], v[72:75]
	v_mfma_f32_16x16x32_bf16 v[96:99], v[154:157], v[200:203], v[96:99]
	v_mfma_f32_16x16x32_bf16 v[92:95], v[178:181], v[200:203], v[92:95]
	v_mfma_f32_16x16x32_bf16 v[84:87], v[178:181], v[208:211], v[84:87]
	v_mfma_f32_16x16x32_bf16 v[88:91], v[154:157], v[208:211], v[88:91]
	v_mfma_f32_16x16x32_bf16 v[80:83], v[154:157], v[216:219], v[80:83]
	v_mfma_f32_16x16x32_bf16 v[76:79], v[178:181], v[216:219], v[76:79]
	v_mfma_f32_16x16x32_bf16 v[68:71], v[178:181], v[228:231], v[68:71]
	v_mfma_f32_16x16x32_bf16 v[72:75], v[154:157], v[228:231], v[72:75]
	s_setprio 2
	s_barrier
	s_add_i32 s68, s68, s42
	s_mov_b64 s[24:25], 0x180
	s_add_i32 s69, s68, 0x2000
	v_lshl_add_u64 v[162:163], v[164:165], 0, s[24:25]
	s_mov_b32 m0, s68
	s_add_u32 s40, s30, 0x40180
	ds_read_b128 v[182:185], v223 offset:49152
	ds_read_b128 v[200:203], v223 offset:50176
	ds_read_b128 v[204:207], v223 offset:51200
	ds_read_b128 v[208:211], v223 offset:52224
	ds_read_b128 v[212:215], v223 offset:53248
	ds_read_b128 v[216:219], v223 offset:54272
	ds_read_b128 v[224:227], v223 offset:55296
	ds_read_b128 v[228:231], v223 offset:56320
	global_load_lds_dwordx4 v[162:163], off
	v_lshl_add_u64 v[162:163], v[166:167], 0, s[24:25]
	s_mov_b32 m0, s69
	s_addc_u32 s41, s31, 0
	s_add_i32 s70, s70, s42
	global_load_lds_dwordx4 v[162:163], off
	v_lshl_add_u64 v[162:163], s[40:41], 0, v[34:35]
	s_mov_b32 m0, s70
	s_add_i32 s71, s70, 0x2000
	global_load_lds_dwordx4 v[162:163], off
	v_lshl_add_u64 v[162:163], s[40:41], 0, v[190:191]
	s_mov_b32 m0, s71
	s_nop 0
	global_load_lds_dwordx4 v[162:163], off
	v_lshl_add_u64 v[162:163], v[168:169], 0, s[24:25]
	s_mov_b32 m0, s51
	s_nop 0
	global_load_lds_dwordx4 v[162:163], off
	v_lshl_add_u64 v[162:163], v[170:171], 0, s[24:25]
	s_mov_b32 m0, s52
	s_nop 0
	global_load_lds_dwordx4 v[162:163], off
	s_waitcnt vmcnt(8)
	s_waitcnt lgkmcnt(0)
	s_barrier
	s_setprio 1
	s_waitcnt lgkmcnt(0)
	v_mfma_f32_16x16x32_bf16 v[64:67], v[134:137], v[182:185], v[64:67]
	v_mfma_f32_16x16x32_bf16 v[60:63], v[142:145], v[182:185], v[60:63]
	v_mfma_f32_16x16x32_bf16 v[52:55], v[142:145], v[204:207], v[52:55]
	v_mfma_f32_16x16x32_bf16 v[56:59], v[134:137], v[204:207], v[56:59]
	v_mfma_f32_16x16x32_bf16 v[48:51], v[134:137], v[212:215], v[48:51]
	v_mfma_f32_16x16x32_bf16 v[44:47], v[142:145], v[212:215], v[44:47]
	v_mfma_f32_16x16x32_bf16 v[36:39], v[142:145], v[224:227], v[36:39]
	v_mfma_f32_16x16x32_bf16 v[40:43], v[134:137], v[224:227], v[40:43]
	v_mfma_f32_16x16x32_bf16 v[64:67], v[138:141], v[200:203], v[64:67]
	v_mfma_f32_16x16x32_bf16 v[60:63], v[146:149], v[200:203], v[60:63]
	v_mfma_f32_16x16x32_bf16 v[52:55], v[146:149], v[208:211], v[52:55]
	v_mfma_f32_16x16x32_bf16 v[56:59], v[138:141], v[208:211], v[56:59]
	v_mfma_f32_16x16x32_bf16 v[48:51], v[138:141], v[216:219], v[48:51]
	v_mfma_f32_16x16x32_bf16 v[44:47], v[146:149], v[216:219], v[44:47]
	v_mfma_f32_16x16x32_bf16 v[36:39], v[146:149], v[228:231], v[36:39]
	v_mfma_f32_16x16x32_bf16 v[40:43], v[138:141], v[228:231], v[40:43]
	s_setprio 2
	s_setprio 1
	v_mfma_f32_16x16x32_bf16 v[30:33], v[150:153], v[182:185], v[30:33]
	v_mfma_f32_16x16x32_bf16 v[26:29], v[158:161], v[182:185], v[26:29]
	v_mfma_f32_16x16x32_bf16 v[18:21], v[158:161], v[204:207], v[18:21]
	v_mfma_f32_16x16x32_bf16 v[22:25], v[150:153], v[204:207], v[22:25]
	v_mfma_f32_16x16x32_bf16 v[14:17], v[150:153], v[212:215], v[14:17]
	v_mfma_f32_16x16x32_bf16 v[10:13], v[158:161], v[212:215], v[10:13]
	v_mfma_f32_16x16x32_bf16 v[2:5], v[158:161], v[224:227], v[2:5]
	v_mfma_f32_16x16x32_bf16 v[6:9], v[150:153], v[224:227], v[6:9]
	v_mfma_f32_16x16x32_bf16 v[30:33], v[154:157], v[200:203], v[30:33]
	v_mfma_f32_16x16x32_bf16 v[26:29], v[178:181], v[200:203], v[26:29]
	v_mfma_f32_16x16x32_bf16 v[18:21], v[178:181], v[208:211], v[18:21]
	v_mfma_f32_16x16x32_bf16 v[22:25], v[154:157], v[208:211], v[22:25]
	v_mfma_f32_16x16x32_bf16 v[14:17], v[154:157], v[216:219], v[14:17]
	v_mfma_f32_16x16x32_bf16 v[10:13], v[178:181], v[216:219], v[10:13]
	v_mfma_f32_16x16x32_bf16 v[2:5], v[178:181], v[228:231], v[2:5]
	v_mfma_f32_16x16x32_bf16 v[6:9], v[154:157], v[228:231], v[6:9]
	s_setprio 2
	s_barrier
	s_add_u32 s36, s36, 0x40180
	s_addc_u32 s37, s37, 0
	s_add_u32 s72, s30, 0x200
	s_addc_u32 s73, s31, 0
	s_mov_b32 s74, 0
	.p2align	6

.LBB0_819:
	s_add_u32 s81, s30, 0x200
	s_addc_u32 s82, s31, 0
	s_add_i32 s55, 0, 0x14000
	s_add_i32 s52, 0, 0x10000
	v_add_u32_e32 v199, s55, v167
	v_add_u32_e32 v200, s52, v167
	ds_read_b128 v[10:13], v199
	ds_read_b128 v[14:17], v199 offset:1024
	ds_read_b128 v[2:5], v199 offset:2048
	ds_read_b128 v[6:9], v199 offset:3072
	ds_read_b128 v[22:25], v200 offset:3072
	ds_read_b128 v[18:21], v200 offset:2048
	ds_read_b128 v[30:33], v200 offset:1024
	ds_read_b128 v[26:29], v200
	s_lshl_b32 s14, s80, 10
	s_add_i32 s83, s14, 0
	s_add_i32 s83, s83, 0x20400
	v_mov_b32_e32 v191, v35
	v_mov_b32_e32 v175, v35
	s_add_i32 s84, s69, 0xc000
	v_readlane_b32 s26, v253, 28
	s_mov_b32 m0, s84
	v_readlane_b32 s27, v253, 29
	s_add_i32 s53, s69, 0xe000
	ds_read_b128 v[202:205], v169
	ds_read_b128 v[206:209], v169 offset:1024
	ds_read_b128 v[222:225], v169 offset:2048
	ds_read_b128 v[226:229], v169 offset:3072
	ds_read_b128 v[230:233], v169 offset:4096
	ds_read_b128 v[234:237], v169 offset:5120
	ds_read_b128 v[238:241], v169 offset:6144
	ds_read_b128 v[242:245], v169 offset:7168
	global_load_lds_dwordx4 v190, s[26:27]
	s_mov_b32 m0, s53
	s_nop 0
	global_load_lds_dwordx4 v174, s[26:27]
	s_waitcnt vmcnt(8)
	s_waitcnt lgkmcnt(0)
	s_barrier
	s_setprio 1
	s_waitcnt lgkmcnt(0)
	v_mfma_f32_16x16x128_f8f6f4 v[160:163], v[26:33], v[202:209], 0
	v_mfma_f32_16x16x128_f8f6f4 v[156:159], v[18:25], v[202:209], 0
	v_mfma_f32_16x16x128_f8f6f4 v[148:151], v[18:25], v[222:229], 0
	v_mfma_f32_16x16x128_f8f6f4 v[152:155], v[26:33], v[222:229], 0
	v_mfma_f32_16x16x128_f8f6f4 v[144:147], v[26:33], v[230:237], 0
	v_mfma_f32_16x16x128_f8f6f4 v[140:143], v[18:25], v[230:237], 0
	v_mfma_f32_16x16x128_f8f6f4 v[132:135], v[18:25], v[238:245], 0
	v_mfma_f32_16x16x128_f8f6f4 v[136:139], v[26:33], v[238:245], 0
	s_setprio 2
	s_setprio 1
	v_mfma_f32_16x16x128_f8f6f4 v[128:131], v[10:17], v[202:209], 0
	v_mfma_f32_16x16x128_f8f6f4 v[124:127], v[2:9], v[202:209], 0
	v_mfma_f32_16x16x128_f8f6f4 v[116:119], v[2:9], v[222:229], 0
	v_mfma_f32_16x16x128_f8f6f4 v[120:123], v[10:17], v[222:229], 0
	v_mfma_f32_16x16x128_f8f6f4 v[112:115], v[10:17], v[230:237], 0
	v_mfma_f32_16x16x128_f8f6f4 v[108:111], v[2:9], v[230:237], 0
	v_mfma_f32_16x16x128_f8f6f4 v[100:103], v[2:9], v[238:245], 0
	v_mfma_f32_16x16x128_f8f6f4 v[104:107], v[10:17], v[238:245], 0
	s_setprio 2
	s_barrier
	s_add_i32 s52, s52, s68
	v_lshl_add_u64 v[194:195], s[30:31], 0, v[170:171]
	s_add_i32 s85, s52, 0x2000
	v_lshl_add_u64 v[178:179], v[194:195], 0, s[28:29]
	s_mov_b32 m0, s52
	v_lshl_add_u64 v[196:197], s[30:31], 0, v[172:173]
	s_add_u32 s36, s30, 0x20100
	ds_read_b128 v[202:205], v169 offset:16384
	ds_read_b128 v[206:209], v169 offset:17408
	ds_read_b128 v[222:225], v169 offset:18432
	ds_read_b128 v[226:229], v169 offset:19456
	ds_read_b128 v[230:233], v169 offset:20480
	ds_read_b128 v[234:237], v169 offset:21504
	ds_read_b128 v[238:241], v169 offset:22528
	ds_read_b128 v[242:245], v169 offset:23552
	global_load_lds_dwordx4 v[178:179], off
	v_lshl_add_u64 v[178:179], v[196:197], 0, s[28:29]
	s_mov_b32 m0, s85
	s_addc_u32 s37, s31, 0
	s_add_i32 s55, s55, s68
	global_load_lds_dwordx4 v[178:179], off
	v_lshl_add_u64 v[178:179], s[36:37], 0, v[170:171]
	s_mov_b32 m0, s55
	s_add_i32 s65, s55, 0x2000
	global_load_lds_dwordx4 v[178:179], off
	v_lshl_add_u64 v[178:179], s[36:37], 0, v[172:173]
	s_mov_b32 m0, s65
	v_readlane_b32 s26, v253, 37
	global_load_lds_dwordx4 v[178:179], off
	s_mov_b32 m0, s69
	v_readlane_b32 s27, v253, 38
	s_nop 4
	global_load_lds_dwordx4 v34, s[26:27]
	s_mov_b32 m0, s70
	s_nop 0
	global_load_lds_dwordx4 v192, s[26:27]
	s_waitcnt vmcnt(8)
	s_waitcnt lgkmcnt(0)
	s_barrier
	s_setprio 1
	s_waitcnt lgkmcnt(0)
	v_mfma_f32_16x16x128_f8f6f4 v[96:99], v[26:33], v[202:209], 0
	v_mfma_f32_16x16x128_f8f6f4 v[92:95], v[18:25], v[202:209], 0
	v_mfma_f32_16x16x128_f8f6f4 v[84:87], v[18:25], v[222:229], 0
	v_mfma_f32_16x16x128_f8f6f4 v[88:91], v[26:33], v[222:229], 0
	v_mfma_f32_16x16x128_f8f6f4 v[80:83], v[26:33], v[230:237], 0
	v_mfma_f32_16x16x128_f8f6f4 v[76:79], v[18:25], v[230:237], 0
	v_mfma_f32_16x16x128_f8f6f4 v[68:71], v[18:25], v[238:245], 0
	v_mfma_f32_16x16x128_f8f6f4 v[72:75], v[26:33], v[238:245], 0
	s_setprio 2
	s_setprio 1
	v_mfma_f32_16x16x128_f8f6f4 v[64:67], v[10:17], v[202:209], 0
	v_mfma_f32_16x16x128_f8f6f4 v[60:63], v[2:9], v[202:209], 0
	v_mfma_f32_16x16x128_f8f6f4 v[52:55], v[2:9], v[222:229], 0
	v_mfma_f32_16x16x128_f8f6f4 v[56:59], v[10:17], v[222:229], 0
	v_mfma_f32_16x16x128_f8f6f4 v[48:51], v[10:17], v[230:237], 0
	v_mfma_f32_16x16x128_f8f6f4 v[44:47], v[2:9], v[230:237], 0
	v_mfma_f32_16x16x128_f8f6f4 v[36:39], v[2:9], v[238:245], 0
	v_mfma_f32_16x16x128_f8f6f4 v[40:43], v[10:17], v[238:245], 0
	s_setprio 2
	s_barrier
	s_add_i32 s54, 0, 0x18000
	s_add_i32 s51, 0, 0x1c000
	v_add_u32_e32 v201, s54, v167
	v_add_u32_e32 v202, s51, v167
	ds_read_b128 v[26:29], v201
	ds_read_b128 v[30:33], v201 offset:1024
	ds_read_b128 v[18:21], v201 offset:2048
	ds_read_b128 v[22:25], v201 offset:3072
	ds_read_b128 v[10:13], v202
	ds_read_b128 v[14:17], v202 offset:1024
	ds_read_b128 v[2:5], v202 offset:2048
	ds_read_b128 v[6:9], v202 offset:3072
	s_mov_b32 m0, s71
	ds_read_b128 v[204:207], v169 offset:32768
	ds_read_b128 v[208:211], v169 offset:33792
	ds_read_b128 v[222:225], v169 offset:34816
	ds_read_b128 v[226:229], v169 offset:35840
	ds_read_b128 v[230:233], v169 offset:36864
	ds_read_b128 v[234:237], v169 offset:37888
	ds_read_b128 v[238:241], v169 offset:38912
	ds_read_b128 v[242:245], v169 offset:39936
	global_load_lds_dwordx4 v189, s[26:27]
	s_mov_b32 m0, s72
	s_nop 0
	global_load_lds_dwordx4 v198, s[26:27]
	s_waitcnt vmcnt(8)
	s_waitcnt lgkmcnt(0)
	s_barrier
	s_setprio 1
	s_waitcnt lgkmcnt(0)
	v_mfma_f32_16x16x128_f8f6f4 v[160:163], v[26:33], v[204:211], v[160:163]
	v_mfma_f32_16x16x128_f8f6f4 v[156:159], v[18:25], v[204:211], v[156:159]
	v_mfma_f32_16x16x128_f8f6f4 v[148:151], v[18:25], v[222:229], v[148:151]
	v_mfma_f32_16x16x128_f8f6f4 v[152:155], v[26:33], v[222:229], v[152:155]
	v_mfma_f32_16x16x128_f8f6f4 v[144:147], v[26:33], v[230:237], v[144:147]
	v_mfma_f32_16x16x128_f8f6f4 v[140:143], v[18:25], v[230:237], v[140:143]
	v_mfma_f32_16x16x128_f8f6f4 v[132:135], v[18:25], v[238:245], v[132:135]
	v_mfma_f32_16x16x128_f8f6f4 v[136:139], v[26:33], v[238:245], v[136:139]
	s_setprio 2
	s_setprio 1
	v_mfma_f32_16x16x128_f8f6f4 v[128:131], v[10:17], v[204:211], v[128:131]
	v_mfma_f32_16x16x128_f8f6f4 v[124:127], v[2:9], v[204:211], v[124:127]
	v_mfma_f32_16x16x128_f8f6f4 v[116:119], v[2:9], v[222:229], v[116:119]
	v_mfma_f32_16x16x128_f8f6f4 v[120:123], v[10:17], v[222:229], v[120:123]
	v_mfma_f32_16x16x128_f8f6f4 v[112:115], v[10:17], v[230:237], v[112:115]
	v_mfma_f32_16x16x128_f8f6f4 v[108:111], v[2:9], v[230:237], v[108:111]
	v_mfma_f32_16x16x128_f8f6f4 v[100:103], v[2:9], v[238:245], v[100:103]
	v_mfma_f32_16x16x128_f8f6f4 v[104:107], v[10:17], v[238:245], v[104:107]
	s_setprio 2
	s_barrier
	s_add_i32 s54, s54, s68
	s_mov_b64 s[26:27], 0x180
	s_add_i32 s50, s54, 0x2000
	v_lshl_add_u64 v[178:179], v[194:195], 0, s[26:27]
	s_mov_b32 m0, s54
	s_add_u32 s30, s30, 0x20180
	ds_read_b128 v[204:207], v169 offset:49152
	ds_read_b128 v[208:211], v169 offset:50176
	ds_read_b128 v[222:225], v169 offset:51200
	ds_read_b128 v[226:229], v169 offset:52224
	ds_read_b128 v[230:233], v169 offset:53248
	ds_read_b128 v[234:237], v169 offset:54272
	ds_read_b128 v[238:241], v169 offset:55296
	ds_read_b128 v[242:245], v169 offset:56320
	global_load_lds_dwordx4 v[178:179], off
	v_lshl_add_u64 v[178:179], v[196:197], 0, s[26:27]
	s_mov_b32 m0, s50
	s_addc_u32 s31, s31, 0
	s_add_i32 s51, s51, s68
	global_load_lds_dwordx4 v[178:179], off
	v_lshl_add_u64 v[178:179], s[30:31], 0, v[170:171]
	s_mov_b32 m0, s51
	s_add_i32 s64, s51, 0x2000
	global_load_lds_dwordx4 v[178:179], off
	v_lshl_add_u64 v[178:179], s[30:31], 0, v[172:173]
	s_mov_b32 m0, s64
	v_readlane_b32 s26, v253, 39
	global_load_lds_dwordx4 v[178:179], off
	s_mov_b32 m0, s75
	v_readlane_b32 s27, v253, 40
	s_nop 4
	global_load_lds_dwordx4 v34, s[26:27]
	s_mov_b32 m0, s76
	s_nop 0
	global_load_lds_dwordx4 v192, s[26:27]
	s_waitcnt vmcnt(8)
	s_waitcnt lgkmcnt(0)
	s_barrier
	s_setprio 1
	s_waitcnt lgkmcnt(0)
	v_mfma_f32_16x16x128_f8f6f4 v[96:99], v[26:33], v[204:211], v[96:99]
	v_mfma_f32_16x16x128_f8f6f4 v[92:95], v[18:25], v[204:211], v[92:95]
	v_mfma_f32_16x16x128_f8f6f4 v[84:87], v[18:25], v[222:229], v[84:87]
	v_mfma_f32_16x16x128_f8f6f4 v[88:91], v[26:33], v[222:229], v[88:91]
	v_mfma_f32_16x16x128_f8f6f4 v[80:83], v[26:33], v[230:237], v[80:83]
	v_mfma_f32_16x16x128_f8f6f4 v[76:79], v[18:25], v[230:237], v[76:79]
	v_mfma_f32_16x16x128_f8f6f4 v[68:71], v[18:25], v[238:245], v[68:71]
	v_mfma_f32_16x16x128_f8f6f4 v[72:75], v[26:33], v[238:245], v[72:75]
	s_setprio 2
	s_setprio 1
	v_mfma_f32_16x16x128_f8f6f4 v[64:67], v[10:17], v[204:211], v[64:67]
	v_mfma_f32_16x16x128_f8f6f4 v[60:63], v[2:9], v[204:211], v[60:63]
	v_mfma_f32_16x16x128_f8f6f4 v[52:55], v[2:9], v[222:229], v[52:55]
	v_mfma_f32_16x16x128_f8f6f4 v[56:59], v[10:17], v[222:229], v[56:59]
	v_mfma_f32_16x16x128_f8f6f4 v[48:51], v[10:17], v[230:237], v[48:51]
	v_mfma_f32_16x16x128_f8f6f4 v[44:47], v[2:9], v[230:237], v[44:47]
	v_mfma_f32_16x16x128_f8f6f4 v[36:39], v[2:9], v[238:245], v[36:39]
	v_mfma_f32_16x16x128_f8f6f4 v[40:43], v[10:17], v[238:245], v[40:43]
	s_setprio 2
	s_barrier
	v_lshl_add_u64 v[18:19], s[26:27], 0, v[174:175]
	v_lshl_add_u64 v[20:21], s[26:27], 0, v[190:191]
	s_mov_b32 s63, 0
	s_mov_b64 s[30:31], 0
	s_branch .LBB0_821
	.p2align	6

.LBB0_899:
	s_mul_i32 s14, s81, 0xe0000
	s_add_u32 s40, s44, s14
	s_addc_u32 s41, s45, 0
	s_and_b64 s[6:7], s[6:7], exec
	s_cselect_b32 s52, s41, s43
	s_cselect_b32 s53, s40, s42
	s_add_i32 s54, 0, 0x10000
	s_add_i32 s65, 0, 0x14000
	v_add_u32_e32 v34, s54, v167
	v_add_u32_e32 v206, s65, v167
	ds_read_b128 v[26:29], v34
	ds_read_b128 v[30:33], v34 offset:1024
	ds_read_b128 v[18:21], v34 offset:2048
	ds_read_b128 v[22:25], v34 offset:3072
	ds_read_b128 v[10:13], v206
	ds_read_b128 v[14:17], v206 offset:1024
	ds_read_b128 v[2:5], v206 offset:2048
	ds_read_b128 v[6:9], v206 offset:3072
	s_add_u32 s6, s42, 0x70080
	s_addc_u32 s7, s43, 0
	s_add_i32 s84, s72, 0xc000
	v_lshl_add_u64 v[216:217], s[6:7], 0, v[174:175]
	s_mov_b32 m0, s84
	s_add_i32 s85, s72, 0xe000
	ds_read_b128 v[178:181], v189
	ds_read_b128 v[182:185], v189 offset:1024
	ds_read_b128 v[198:201], v189 offset:2048
	ds_read_b128 v[202:205], v189 offset:3072
	ds_read_b128 v[208:211], v189 offset:4096
	ds_read_b128 v[212:215], v189 offset:5120
	ds_read_b128 v[222:225], v189 offset:6144
	ds_read_b128 v[226:229], v189 offset:7168
	global_load_lds_dwordx4 v[216:217], off
	v_lshl_add_u64 v[216:217], s[6:7], 0, v[170:171]
	s_mov_b32 m0, s85
	s_nop 0
	global_load_lds_dwordx4 v[216:217], off
	s_waitcnt vmcnt(8)
	s_waitcnt lgkmcnt(0)
	s_barrier
	s_setprio 1
	s_waitcnt lgkmcnt(0)
	v_mfma_f32_16x16x128_f8f6f4 v[160:163], v[26:33], v[178:185], 0
	v_mfma_f32_16x16x128_f8f6f4 v[156:159], v[18:25], v[178:185], 0
	v_mfma_f32_16x16x128_f8f6f4 v[148:151], v[18:25], v[198:205], 0
	v_mfma_f32_16x16x128_f8f6f4 v[152:155], v[26:33], v[198:205], 0
	v_mfma_f32_16x16x128_f8f6f4 v[144:147], v[26:33], v[208:215], 0
	v_mfma_f32_16x16x128_f8f6f4 v[140:143], v[18:25], v[208:215], 0
	v_mfma_f32_16x16x128_f8f6f4 v[132:135], v[18:25], v[222:229], 0
	v_mfma_f32_16x16x128_f8f6f4 v[136:139], v[26:33], v[222:229], 0
	s_setprio 2
	s_setprio 1
	v_mfma_f32_16x16x128_f8f6f4 v[128:131], v[10:17], v[178:185], 0
	v_mfma_f32_16x16x128_f8f6f4 v[124:127], v[2:9], v[178:185], 0
	v_mfma_f32_16x16x128_f8f6f4 v[116:119], v[2:9], v[198:205], 0
	v_mfma_f32_16x16x128_f8f6f4 v[120:123], v[10:17], v[198:205], 0
	v_mfma_f32_16x16x128_f8f6f4 v[112:115], v[10:17], v[208:215], 0
	v_mfma_f32_16x16x128_f8f6f4 v[108:111], v[2:9], v[208:215], 0
	v_mfma_f32_16x16x128_f8f6f4 v[100:103], v[2:9], v[222:229], 0
	v_mfma_f32_16x16x128_f8f6f4 v[104:107], v[10:17], v[222:229], 0
	s_setprio 2
	s_barrier
	v_lshl_add_u64 v[198:199], v[196:197], 0, v[172:173]
	s_add_i32 s54, s54, s71
	v_lshl_add_u64 v[200:201], v[198:199], 0, s[28:29]
	s_mov_b32 m0, s54
	ds_read_b128 v[178:181], v189 offset:16384
	ds_read_b128 v[182:185], v189 offset:17408
	ds_read_b128 v[208:211], v189 offset:18432
	ds_read_b128 v[212:215], v189 offset:19456
	ds_read_b128 v[222:225], v189 offset:20480
	ds_read_b128 v[226:229], v189 offset:21504
	ds_read_b128 v[230:233], v189 offset:22528
	ds_read_b128 v[234:237], v189 offset:23552
	global_load_lds_dwordx4 v[200:201], off
	v_lshl_add_u64 v[200:201], v[196:197], 0, v[168:169]
	s_add_i32 s55, s54, 0x2000
	v_lshl_add_u64 v[202:203], v[200:201], 0, s[28:29]
	s_mov_b32 m0, s55
	s_mov_b64 s[6:7], 0x70100
	global_load_lds_dwordx4 v[202:203], off
	v_lshl_add_u64 v[202:203], v[196:197], 0, s[6:7]
	s_add_i32 s65, s65, s71
	v_lshl_add_u64 v[204:205], v[202:203], 0, v[172:173]
	s_mov_b32 m0, s65
	s_add_i32 s67, s65, 0x2000
	global_load_lds_dwordx4 v[204:205], off
	v_lshl_add_u64 v[202:203], v[202:203], 0, v[168:169]
	s_mov_b32 m0, s67
	s_nop 0
	global_load_lds_dwordx4 v[202:203], off
	v_lshl_add_u64 v[202:203], s[42:43], 0, v[174:175]
	v_lshl_add_u64 v[204:205], v[202:203], 0, s[28:29]
	s_mov_b32 m0, s72
	s_nop 0
	global_load_lds_dwordx4 v[204:205], off
	v_lshl_add_u64 v[204:205], s[42:43], 0, v[170:171]
	v_lshl_add_u64 v[216:217], v[204:205], 0, s[28:29]
	s_mov_b32 m0, s73
	s_nop 0
	global_load_lds_dwordx4 v[216:217], off
	s_waitcnt vmcnt(8)
	s_waitcnt lgkmcnt(0)
	s_barrier
	s_setprio 1
	s_waitcnt lgkmcnt(0)
	v_mfma_f32_16x16x128_f8f6f4 v[96:99], v[26:33], v[178:185], 0
	v_mfma_f32_16x16x128_f8f6f4 v[92:95], v[18:25], v[178:185], 0
	v_mfma_f32_16x16x128_f8f6f4 v[84:87], v[18:25], v[208:215], 0
	v_mfma_f32_16x16x128_f8f6f4 v[88:91], v[26:33], v[208:215], 0
	v_mfma_f32_16x16x128_f8f6f4 v[80:83], v[26:33], v[222:229], 0
	v_mfma_f32_16x16x128_f8f6f4 v[76:79], v[18:25], v[222:229], 0
	v_mfma_f32_16x16x128_f8f6f4 v[68:71], v[18:25], v[230:237], 0
	v_mfma_f32_16x16x128_f8f6f4 v[72:75], v[26:33], v[230:237], 0
	s_setprio 2
	s_setprio 1
	v_mfma_f32_16x16x128_f8f6f4 v[64:67], v[10:17], v[178:185], 0
	v_mfma_f32_16x16x128_f8f6f4 v[60:63], v[2:9], v[178:185], 0
	v_mfma_f32_16x16x128_f8f6f4 v[52:55], v[2:9], v[208:215], 0
	v_mfma_f32_16x16x128_f8f6f4 v[56:59], v[10:17], v[208:215], 0
	v_mfma_f32_16x16x128_f8f6f4 v[48:51], v[10:17], v[222:229], 0
	v_mfma_f32_16x16x128_f8f6f4 v[44:47], v[2:9], v[222:229], 0
	v_mfma_f32_16x16x128_f8f6f4 v[36:39], v[2:9], v[230:237], 0
	v_mfma_f32_16x16x128_f8f6f4 v[40:43], v[10:17], v[230:237], 0
	s_setprio 2
	s_barrier
	s_add_i32 s50, 0, 0x18000
	s_add_i32 s63, 0, 0x1c000
	v_add_u32_e32 v207, s50, v167
	v_add_u32_e32 v208, s63, v167
	ds_read_b128 v[26:29], v207
	ds_read_b128 v[30:33], v207 offset:1024
	ds_read_b128 v[18:21], v207 offset:2048
	ds_read_b128 v[22:25], v207 offset:3072
	ds_read_b128 v[10:13], v208
	ds_read_b128 v[14:17], v208 offset:1024
	ds_read_b128 v[2:5], v208 offset:2048
	ds_read_b128 v[6:9], v208 offset:3072
	s_add_u32 s6, s42, 0x70100
	s_addc_u32 s7, s43, 0
	s_mov_b32 m0, s74
	v_lshl_add_u64 v[218:219], s[6:7], 0, v[174:175]
	ds_read_b128 v[178:181], v189 offset:32768
	ds_read_b128 v[182:185], v189 offset:33792
	ds_read_b128 v[210:213], v189 offset:34816
	ds_read_b128 v[214:217], v189 offset:35840
	ds_read_b128 v[222:225], v189 offset:36864
	ds_read_b128 v[226:229], v189 offset:37888
	ds_read_b128 v[230:233], v189 offset:38912
	ds_read_b128 v[234:237], v189 offset:39936
	global_load_lds_dwordx4 v[218:219], off
	v_lshl_add_u64 v[218:219], s[6:7], 0, v[170:171]
	s_mov_b32 m0, s75
	s_nop 0
	global_load_lds_dwordx4 v[218:219], off
	s_waitcnt vmcnt(8)
	s_waitcnt lgkmcnt(0)
	s_barrier
	s_setprio 1
	s_waitcnt lgkmcnt(0)
	v_mfma_f32_16x16x128_f8f6f4 v[160:163], v[26:33], v[178:185], v[160:163]
	v_mfma_f32_16x16x128_f8f6f4 v[156:159], v[18:25], v[178:185], v[156:159]
	v_mfma_f32_16x16x128_f8f6f4 v[148:151], v[18:25], v[210:217], v[148:151]
	v_mfma_f32_16x16x128_f8f6f4 v[152:155], v[26:33], v[210:217], v[152:155]
	v_mfma_f32_16x16x128_f8f6f4 v[144:147], v[26:33], v[222:229], v[144:147]
	v_mfma_f32_16x16x128_f8f6f4 v[140:143], v[18:25], v[222:229], v[140:143]
	v_mfma_f32_16x16x128_f8f6f4 v[132:135], v[18:25], v[230:237], v[132:135]
	v_mfma_f32_16x16x128_f8f6f4 v[136:139], v[26:33], v[230:237], v[136:139]
	s_setprio 2
	s_setprio 1
	v_mfma_f32_16x16x128_f8f6f4 v[128:131], v[10:17], v[178:185], v[128:131]
	v_mfma_f32_16x16x128_f8f6f4 v[124:127], v[2:9], v[178:185], v[124:127]
	v_mfma_f32_16x16x128_f8f6f4 v[116:119], v[2:9], v[210:217], v[116:119]
	v_mfma_f32_16x16x128_f8f6f4 v[120:123], v[10:17], v[210:217], v[120:123]
	v_mfma_f32_16x16x128_f8f6f4 v[112:115], v[10:17], v[222:229], v[112:115]
	v_mfma_f32_16x16x128_f8f6f4 v[108:111], v[2:9], v[222:229], v[108:111]
	v_mfma_f32_16x16x128_f8f6f4 v[100:103], v[2:9], v[230:237], v[100:103]
	v_mfma_f32_16x16x128_f8f6f4 v[104:107], v[10:17], v[230:237], v[104:107]
	s_setprio 2
	s_barrier
	s_mov_b64 s[6:7], 0x180
	s_add_i32 s50, s50, s71
	v_lshl_add_u64 v[198:199], v[198:199], 0, s[6:7]
	s_mov_b32 m0, s50
	s_add_i32 s51, s50, 0x2000
	ds_read_b128 v[178:181], v189 offset:49152
	ds_read_b128 v[182:185], v189 offset:50176
	ds_read_b128 v[210:213], v189 offset:51200
	ds_read_b128 v[214:217], v189 offset:52224
	ds_read_b128 v[222:225], v189 offset:53248
	ds_read_b128 v[226:229], v189 offset:54272
	ds_read_b128 v[230:233], v189 offset:55296
	ds_read_b128 v[234:237], v189 offset:56320
	global_load_lds_dwordx4 v[198:199], off
	v_lshl_add_u64 v[198:199], v[200:201], 0, s[6:7]
	s_mov_b32 m0, s51
	s_add_i32 s63, s63, s71
	global_load_lds_dwordx4 v[198:199], off
	v_lshl_add_u64 v[198:199], v[196:197], 0, s[26:27]
	v_lshl_add_u64 v[200:201], v[198:199], 0, v[172:173]
	s_mov_b32 m0, s63
	s_add_i32 s64, s63, 0x2000
	global_load_lds_dwordx4 v[200:201], off
	v_lshl_add_u64 v[198:199], v[198:199], 0, v[168:169]
	s_mov_b32 m0, s64
	s_nop 0
	global_load_lds_dwordx4 v[198:199], off
	v_lshl_add_u64 v[198:199], v[202:203], 0, s[6:7]
	s_mov_b32 m0, s77
	s_nop 0
	global_load_lds_dwordx4 v[198:199], off
	v_lshl_add_u64 v[198:199], v[204:205], 0, s[6:7]
	s_mov_b32 m0, s78
	s_nop 0
	global_load_lds_dwordx4 v[198:199], off
	s_waitcnt vmcnt(8)
	s_waitcnt lgkmcnt(0)
	s_barrier
	s_setprio 1
	s_waitcnt lgkmcnt(0)
	v_mfma_f32_16x16x128_f8f6f4 v[96:99], v[26:33], v[178:185], v[96:99]
	v_mfma_f32_16x16x128_f8f6f4 v[92:95], v[18:25], v[178:185], v[92:95]
	v_mfma_f32_16x16x128_f8f6f4 v[84:87], v[18:25], v[210:217], v[84:87]
	v_mfma_f32_16x16x128_f8f6f4 v[88:91], v[26:33], v[210:217], v[88:91]
	v_mfma_f32_16x16x128_f8f6f4 v[80:83], v[26:33], v[222:229], v[80:83]
	v_mfma_f32_16x16x128_f8f6f4 v[76:79], v[18:25], v[222:229], v[76:79]
	v_mfma_f32_16x16x128_f8f6f4 v[68:71], v[18:25], v[230:237], v[68:71]
	v_mfma_f32_16x16x128_f8f6f4 v[72:75], v[26:33], v[230:237], v[72:75]
	s_setprio 2
	s_setprio 1
	v_mfma_f32_16x16x128_f8f6f4 v[64:67], v[10:17], v[178:185], v[64:67]
	v_mfma_f32_16x16x128_f8f6f4 v[60:63], v[2:9], v[178:185], v[60:63]
	v_mfma_f32_16x16x128_f8f6f4 v[52:55], v[2:9], v[210:217], v[52:55]
	v_mfma_f32_16x16x128_f8f6f4 v[56:59], v[10:17], v[210:217], v[56:59]
	v_mfma_f32_16x16x128_f8f6f4 v[48:51], v[10:17], v[222:229], v[48:51]
	v_mfma_f32_16x16x128_f8f6f4 v[44:47], v[2:9], v[222:229], v[44:47]
	v_mfma_f32_16x16x128_f8f6f4 v[36:39], v[2:9], v[230:237], v[36:39]
	v_mfma_f32_16x16x128_f8f6f4 v[40:43], v[10:17], v[230:237], v[40:43]
	s_setprio 2
	s_barrier
	s_mov_b64 s[6:7], 0x200
	v_lshl_add_u64 v[18:19], v[196:197], 0, s[6:7]
	s_mov_b32 s86, 0
	.p2align	6

.LBB0_953:
	s_add_u32 s95, s30, 0x200
	s_addc_u32 s96, s31, 0
	s_add_i32 s65, 0, 0x14000
	s_add_i32 s67, 0, 0x10000
	v_add_u32_e32 v199, s65, v167
	v_add_u32_e32 v200, s67, v167
	ds_read_b128 v[10:13], v199
	ds_read_b128 v[14:17], v199 offset:1024
	ds_read_b128 v[2:5], v199 offset:2048
	ds_read_b128 v[6:9], v199 offset:3072
	ds_read_b128 v[22:25], v200 offset:3072
	ds_read_b128 v[18:21], v200 offset:2048
	ds_read_b128 v[30:33], v200 offset:1024
	ds_read_b128 v[26:29], v200
	s_lshl_b32 s14, s94, 10
	s_add_i32 s97, s14, 0
	s_add_i32 s97, s97, 0x20400
	v_mov_b32_e32 v191, v35
	v_mov_b32_e32 v175, v35
	s_add_i32 s83, s52, 0xc000
	v_readlane_b32 s26, v253, 28
	s_mov_b32 m0, s83
	v_readlane_b32 s27, v253, 29
	s_add_i32 s53, s52, 0xe000
	ds_read_b128 v[178:181], v169
	ds_read_b128 v[182:185], v169 offset:1024
	ds_read_b128 v[202:205], v169 offset:2048
	ds_read_b128 v[206:209], v169 offset:3072
	ds_read_b128 v[210:213], v169 offset:4096
	ds_read_b128 v[214:217], v169 offset:5120
	ds_read_b128 v[222:225], v169 offset:6144
	ds_read_b128 v[226:229], v169 offset:7168
	global_load_lds_dwordx4 v190, s[26:27]
	s_mov_b32 m0, s53
	s_nop 0
	global_load_lds_dwordx4 v174, s[26:27]
	s_waitcnt vmcnt(8)
	s_waitcnt lgkmcnt(0)
	s_barrier
	s_setprio 1
	s_waitcnt lgkmcnt(0)
	v_mfma_f32_16x16x128_f8f6f4 v[160:163], v[26:33], v[178:185], 0
	v_mfma_f32_16x16x128_f8f6f4 v[156:159], v[18:25], v[178:185], 0
	v_mfma_f32_16x16x128_f8f6f4 v[148:151], v[18:25], v[202:209], 0
	v_mfma_f32_16x16x128_f8f6f4 v[152:155], v[26:33], v[202:209], 0
	v_mfma_f32_16x16x128_f8f6f4 v[144:147], v[26:33], v[210:217], 0
	v_mfma_f32_16x16x128_f8f6f4 v[140:143], v[18:25], v[210:217], 0
	v_mfma_f32_16x16x128_f8f6f4 v[132:135], v[18:25], v[222:229], 0
	v_mfma_f32_16x16x128_f8f6f4 v[136:139], v[26:33], v[222:229], 0
	s_setprio 2
	s_setprio 1
	v_mfma_f32_16x16x128_f8f6f4 v[128:131], v[10:17], v[178:185], 0
	v_mfma_f32_16x16x128_f8f6f4 v[124:127], v[2:9], v[178:185], 0
	v_mfma_f32_16x16x128_f8f6f4 v[116:119], v[2:9], v[202:209], 0
	v_mfma_f32_16x16x128_f8f6f4 v[120:123], v[10:17], v[202:209], 0
	v_mfma_f32_16x16x128_f8f6f4 v[112:115], v[10:17], v[210:217], 0
	v_mfma_f32_16x16x128_f8f6f4 v[108:111], v[2:9], v[210:217], 0
	v_mfma_f32_16x16x128_f8f6f4 v[100:103], v[2:9], v[222:229], 0
	v_mfma_f32_16x16x128_f8f6f4 v[104:107], v[10:17], v[222:229], 0
	s_setprio 2
	s_barrier
	v_lshl_add_u64 v[194:195], s[30:31], 0, v[170:171]
	s_add_i32 s67, s67, s82
	v_lshl_add_u64 v[196:197], v[194:195], 0, s[28:29]
	s_mov_b32 m0, s67
	s_add_i32 s55, s67, 0x2000
	ds_read_b128 v[178:181], v169 offset:16384
	ds_read_b128 v[182:185], v169 offset:17408
	ds_read_b128 v[202:205], v169 offset:18432
	ds_read_b128 v[206:209], v169 offset:19456
	ds_read_b128 v[210:213], v169 offset:20480
	ds_read_b128 v[214:217], v169 offset:21504
	ds_read_b128 v[222:225], v169 offset:22528
	ds_read_b128 v[226:229], v169 offset:23552
	global_load_lds_dwordx4 v[196:197], off
	v_lshl_add_u64 v[196:197], s[30:31], 0, v[172:173]
	s_add_u32 s46, s30, 0x20100
	v_lshl_add_u64 v[218:219], v[196:197], 0, s[28:29]
	s_mov_b32 m0, s55
	s_addc_u32 s47, s31, 0
	s_add_i32 s65, s65, s82
	global_load_lds_dwordx4 v[218:219], off
	v_lshl_add_u64 v[218:219], s[46:47], 0, v[170:171]
	s_mov_b32 m0, s65
	s_add_i32 s54, s65, 0x2000
	global_load_lds_dwordx4 v[218:219], off
	v_lshl_add_u64 v[218:219], s[46:47], 0, v[172:173]
	s_mov_b32 m0, s54
	v_readlane_b32 s26, v253, 37
	global_load_lds_dwordx4 v[218:219], off
	s_mov_b32 m0, s52
	v_readlane_b32 s27, v253, 38
	s_nop 4
	global_load_lds_dwordx4 v34, s[26:27]
	s_mov_b32 m0, s84
	s_nop 0
	global_load_lds_dwordx4 v192, s[26:27]
	s_waitcnt vmcnt(8)
	s_waitcnt lgkmcnt(0)
	s_barrier
	s_setprio 1
	s_waitcnt lgkmcnt(0)
	v_mfma_f32_16x16x128_f8f6f4 v[96:99], v[26:33], v[178:185], 0
	v_mfma_f32_16x16x128_f8f6f4 v[92:95], v[18:25], v[178:185], 0
	v_mfma_f32_16x16x128_f8f6f4 v[84:87], v[18:25], v[202:209], 0
	v_mfma_f32_16x16x128_f8f6f4 v[88:91], v[26:33], v[202:209], 0
	v_mfma_f32_16x16x128_f8f6f4 v[80:83], v[26:33], v[210:217], 0
	v_mfma_f32_16x16x128_f8f6f4 v[76:79], v[18:25], v[210:217], 0
	v_mfma_f32_16x16x128_f8f6f4 v[68:71], v[18:25], v[222:229], 0
	v_mfma_f32_16x16x128_f8f6f4 v[72:75], v[26:33], v[222:229], 0
	s_setprio 2
	s_setprio 1
	v_mfma_f32_16x16x128_f8f6f4 v[64:67], v[10:17], v[178:185], 0
	v_mfma_f32_16x16x128_f8f6f4 v[60:63], v[2:9], v[178:185], 0
	v_mfma_f32_16x16x128_f8f6f4 v[52:55], v[2:9], v[202:209], 0
	v_mfma_f32_16x16x128_f8f6f4 v[56:59], v[10:17], v[202:209], 0
	v_mfma_f32_16x16x128_f8f6f4 v[48:51], v[10:17], v[210:217], 0
	v_mfma_f32_16x16x128_f8f6f4 v[44:47], v[2:9], v[210:217], 0
	v_mfma_f32_16x16x128_f8f6f4 v[36:39], v[2:9], v[222:229], 0
	v_mfma_f32_16x16x128_f8f6f4 v[40:43], v[10:17], v[222:229], 0
	s_setprio 2
	s_barrier
	s_add_i32 s50, 0, 0x18000
	s_add_i32 s64, 0, 0x1c000
	v_add_u32_e32 v201, s50, v167
	v_add_u32_e32 v202, s64, v167
	ds_read_b128 v[26:29], v201
	ds_read_b128 v[30:33], v201 offset:1024
	ds_read_b128 v[18:21], v201 offset:2048
	ds_read_b128 v[22:25], v201 offset:3072
	ds_read_b128 v[10:13], v202
	ds_read_b128 v[14:17], v202 offset:1024
	ds_read_b128 v[2:5], v202 offset:2048
	ds_read_b128 v[6:9], v202 offset:3072
	s_mov_b32 m0, s85
	ds_read_b128 v[178:181], v169 offset:32768
	ds_read_b128 v[182:185], v169 offset:33792
	ds_read_b128 v[204:207], v169 offset:34816
	ds_read_b128 v[208:211], v169 offset:35840
	ds_read_b128 v[212:215], v169 offset:36864
	ds_read_b128 v[216:219], v169 offset:37888
	ds_read_b128 v[222:225], v169 offset:38912
	ds_read_b128 v[226:229], v169 offset:39936
	global_load_lds_dwordx4 v189, s[26:27]
	s_mov_b32 m0, s86
	s_nop 0
	global_load_lds_dwordx4 v198, s[26:27]
	s_waitcnt vmcnt(8)
	s_waitcnt lgkmcnt(0)
	s_barrier
	s_setprio 1
	s_waitcnt lgkmcnt(0)
	v_mfma_f32_16x16x128_f8f6f4 v[160:163], v[26:33], v[178:185], v[160:163]
	v_mfma_f32_16x16x128_f8f6f4 v[156:159], v[18:25], v[178:185], v[156:159]
	v_mfma_f32_16x16x128_f8f6f4 v[148:151], v[18:25], v[204:211], v[148:151]
	v_mfma_f32_16x16x128_f8f6f4 v[152:155], v[26:33], v[204:211], v[152:155]
	v_mfma_f32_16x16x128_f8f6f4 v[144:147], v[26:33], v[212:219], v[144:147]
	v_mfma_f32_16x16x128_f8f6f4 v[140:143], v[18:25], v[212:219], v[140:143]
	v_mfma_f32_16x16x128_f8f6f4 v[132:135], v[18:25], v[222:229], v[132:135]
	v_mfma_f32_16x16x128_f8f6f4 v[136:139], v[26:33], v[222:229], v[136:139]
	s_setprio 2
	s_setprio 1
	v_mfma_f32_16x16x128_f8f6f4 v[128:131], v[10:17], v[178:185], v[128:131]
	v_mfma_f32_16x16x128_f8f6f4 v[124:127], v[2:9], v[178:185], v[124:127]
	v_mfma_f32_16x16x128_f8f6f4 v[116:119], v[2:9], v[204:211], v[116:119]
	v_mfma_f32_16x16x128_f8f6f4 v[120:123], v[10:17], v[204:211], v[120:123]
	v_mfma_f32_16x16x128_f8f6f4 v[112:115], v[10:17], v[212:219], v[112:115]
	v_mfma_f32_16x16x128_f8f6f4 v[108:111], v[2:9], v[212:219], v[108:111]
	v_mfma_f32_16x16x128_f8f6f4 v[100:103], v[2:9], v[222:229], v[100:103]
	v_mfma_f32_16x16x128_f8f6f4 v[104:107], v[10:17], v[222:229], v[104:107]
	s_setprio 2
	s_barrier
	s_add_i32 s50, s50, s82
	s_mov_b64 s[26:27], 0x180
	s_add_i32 s51, s50, 0x2000
	v_lshl_add_u64 v[194:195], v[194:195], 0, s[26:27]
	s_mov_b32 m0, s50
	s_add_u32 s30, s30, 0x20180
	ds_read_b128 v[178:181], v169 offset:49152
	ds_read_b128 v[182:185], v169 offset:50176
	ds_read_b128 v[204:207], v169 offset:51200
	ds_read_b128 v[208:211], v169 offset:52224
	ds_read_b128 v[212:215], v169 offset:53248
	ds_read_b128 v[216:219], v169 offset:54272
	ds_read_b128 v[222:225], v169 offset:55296
	ds_read_b128 v[226:229], v169 offset:56320
	global_load_lds_dwordx4 v[194:195], off
	v_lshl_add_u64 v[194:195], v[196:197], 0, s[26:27]
	s_mov_b32 m0, s51
	s_addc_u32 s31, s31, 0
	s_add_i32 s64, s64, s82
	global_load_lds_dwordx4 v[194:195], off
	v_lshl_add_u64 v[194:195], s[30:31], 0, v[170:171]
	s_mov_b32 m0, s64
	s_add_i32 s63, s64, 0x2000
	global_load_lds_dwordx4 v[194:195], off
	v_lshl_add_u64 v[194:195], s[30:31], 0, v[172:173]
	s_mov_b32 m0, s63
	v_readlane_b32 s26, v253, 39
	global_load_lds_dwordx4 v[194:195], off
	s_mov_b32 m0, s90
	v_readlane_b32 s27, v253, 40
	s_nop 4
	global_load_lds_dwordx4 v34, s[26:27]
	s_mov_b32 m0, s91
	s_nop 0
	global_load_lds_dwordx4 v192, s[26:27]
	s_waitcnt vmcnt(8)
	s_waitcnt lgkmcnt(0)
	s_barrier
	s_setprio 1
	s_waitcnt lgkmcnt(0)
	v_mfma_f32_16x16x128_f8f6f4 v[96:99], v[26:33], v[178:185], v[96:99]
	v_mfma_f32_16x16x128_f8f6f4 v[92:95], v[18:25], v[178:185], v[92:95]
	v_mfma_f32_16x16x128_f8f6f4 v[84:87], v[18:25], v[204:211], v[84:87]
	v_mfma_f32_16x16x128_f8f6f4 v[88:91], v[26:33], v[204:211], v[88:91]
	v_mfma_f32_16x16x128_f8f6f4 v[80:83], v[26:33], v[212:219], v[80:83]
	v_mfma_f32_16x16x128_f8f6f4 v[76:79], v[18:25], v[212:219], v[76:79]
	v_mfma_f32_16x16x128_f8f6f4 v[68:71], v[18:25], v[222:229], v[68:71]
	v_mfma_f32_16x16x128_f8f6f4 v[72:75], v[26:33], v[222:229], v[72:75]
	s_setprio 2
	s_setprio 1
	v_mfma_f32_16x16x128_f8f6f4 v[64:67], v[10:17], v[178:185], v[64:67]
	v_mfma_f32_16x16x128_f8f6f4 v[60:63], v[2:9], v[178:185], v[60:63]
	v_mfma_f32_16x16x128_f8f6f4 v[52:55], v[2:9], v[204:211], v[52:55]
	v_mfma_f32_16x16x128_f8f6f4 v[56:59], v[10:17], v[204:211], v[56:59]
	v_mfma_f32_16x16x128_f8f6f4 v[48:51], v[10:17], v[212:219], v[48:51]
	v_mfma_f32_16x16x128_f8f6f4 v[44:47], v[2:9], v[212:219], v[44:47]
	v_mfma_f32_16x16x128_f8f6f4 v[36:39], v[2:9], v[222:229], v[36:39]
	v_mfma_f32_16x16x128_f8f6f4 v[40:43], v[10:17], v[222:229], v[40:43]
	s_setprio 2
	s_barrier
	v_lshl_add_u64 v[18:19], s[26:27], 0, v[174:175]
	v_lshl_add_u64 v[20:21], s[26:27], 0, v[190:191]
	s_mov_b32 s75, 0
	s_mov_b64 s[30:31], 0
	s_branch .LBB0_955
	.p2align	6

.LBB0_1086:
	s_lshl_b32 s10, s51, 18
	s_add_u32 s10, s20, s10
	s_addc_u32 s11, s21, 0
	s_and_b64 s[16:17], s[4:5], exec
	s_cselect_b32 s54, s11, s31
	s_cselect_b32 s55, s10, s30
	s_lshl_b32 s14, s50, 18
	s_add_u32 s16, s15, s14
	s_addc_u32 s17, s26, 0
	s_and_b64 s[36:37], s[4:5], exec
	s_cselect_b32 s56, s17, s23
	s_cselect_b32 s57, s16, s22
	s_add_i32 s60, 0, 0x10000
	s_add_i32 s62, 0, 0x14000
	v_add_u32_e32 v198, s60, v196
	v_add_u32_e32 v199, s62, v196
	ds_read_b128 v[26:29], v198
	ds_read_b128 v[30:33], v198 offset:1024
	ds_read_b128 v[18:21], v198 offset:2048
	ds_read_b128 v[22:25], v198 offset:3072
	ds_read_b128 v[10:13], v199
	ds_read_b128 v[14:17], v199 offset:1024
	ds_read_b128 v[2:5], v199 offset:2048
	ds_read_b128 v[6:9], v199 offset:3072
	s_add_u32 s36, s30, 0x20080
	s_addc_u32 s37, s31, 0
	s_add_i32 s58, s41, 0xc000
	v_lshl_add_u64 v[174:175], s[36:37], 0, v[168:169]
	s_mov_b32 m0, s58
	s_add_i32 s59, s41, 0xe000
	ds_read_b128 v[200:203], v197
	ds_read_b128 v[204:207], v197 offset:1024
	ds_read_b128 v[222:225], v197 offset:2048
	ds_read_b128 v[226:229], v197 offset:3072
	ds_read_b128 v[230:233], v197 offset:4096
	ds_read_b128 v[234:237], v197 offset:5120
	ds_read_b128 v[238:241], v197 offset:6144
	ds_read_b128 v[242:245], v197 offset:7168
	global_load_lds_dwordx4 v[174:175], off
	v_lshl_add_u64 v[174:175], s[36:37], 0, v[166:167]
	s_mov_b32 m0, s59
	s_nop 0
	global_load_lds_dwordx4 v[174:175], off
	s_waitcnt vmcnt(8)
	s_waitcnt lgkmcnt(0)
	s_barrier
	s_setprio 1
	s_waitcnt lgkmcnt(0)
	v_mfma_f32_16x16x128_f8f6f4 v[160:163], v[26:33], v[200:207], 0
	v_mfma_f32_16x16x128_f8f6f4 v[156:159], v[18:25], v[200:207], 0
	v_mfma_f32_16x16x128_f8f6f4 v[148:151], v[18:25], v[222:229], 0
	v_mfma_f32_16x16x128_f8f6f4 v[152:155], v[26:33], v[222:229], 0
	v_mfma_f32_16x16x128_f8f6f4 v[144:147], v[26:33], v[230:237], 0
	v_mfma_f32_16x16x128_f8f6f4 v[140:143], v[18:25], v[230:237], 0
	v_mfma_f32_16x16x128_f8f6f4 v[132:135], v[18:25], v[238:245], 0
	v_mfma_f32_16x16x128_f8f6f4 v[136:139], v[26:33], v[238:245], 0
	s_setprio 2
	s_setprio 1
	v_mfma_f32_16x16x128_f8f6f4 v[128:131], v[10:17], v[200:207], 0
	v_mfma_f32_16x16x128_f8f6f4 v[124:127], v[2:9], v[200:207], 0
	v_mfma_f32_16x16x128_f8f6f4 v[116:119], v[2:9], v[222:229], 0
	v_mfma_f32_16x16x128_f8f6f4 v[120:123], v[10:17], v[222:229], 0
	v_mfma_f32_16x16x128_f8f6f4 v[112:115], v[10:17], v[230:237], 0
	v_mfma_f32_16x16x128_f8f6f4 v[108:111], v[2:9], v[230:237], 0
	v_mfma_f32_16x16x128_f8f6f4 v[100:103], v[2:9], v[238:245], 0
	v_mfma_f32_16x16x128_f8f6f4 v[104:107], v[10:17], v[238:245], 0
	s_setprio 2
	s_barrier
	s_add_i32 s60, s60, s40
	v_lshl_add_u64 v[174:175], s[22:23], 0, v[34:35]
	s_add_i32 s61, s60, 0x2000
	v_lshl_add_u64 v[178:179], v[174:175], 0, s[28:29]
	s_mov_b32 m0, s60
	v_lshl_add_u64 v[190:191], s[22:23], 0, v[164:165]
	s_add_u32 s36, s22, 0x20100
	ds_read_b128 v[200:203], v197 offset:16384
	ds_read_b128 v[204:207], v197 offset:17408
	ds_read_b128 v[222:225], v197 offset:18432
	ds_read_b128 v[226:229], v197 offset:19456
	ds_read_b128 v[230:233], v197 offset:20480
	ds_read_b128 v[234:237], v197 offset:21504
	ds_read_b128 v[238:241], v197 offset:22528
	ds_read_b128 v[242:245], v197 offset:23552
	global_load_lds_dwordx4 v[178:179], off
	v_lshl_add_u64 v[178:179], v[190:191], 0, s[28:29]
	s_mov_b32 m0, s61
	s_addc_u32 s37, s23, 0
	s_add_i32 s62, s62, s40
	global_load_lds_dwordx4 v[178:179], off
	v_lshl_add_u64 v[178:179], s[36:37], 0, v[34:35]
	s_mov_b32 m0, s62
	s_add_i32 s63, s62, 0x2000
	global_load_lds_dwordx4 v[178:179], off
	v_lshl_add_u64 v[178:179], s[36:37], 0, v[164:165]
	s_mov_b32 m0, s63
	v_lshl_add_u64 v[192:193], s[30:31], 0, v[168:169]
	global_load_lds_dwordx4 v[178:179], off
	v_lshl_add_u64 v[178:179], v[192:193], 0, s[28:29]
	s_mov_b32 m0, s41
	v_lshl_add_u64 v[194:195], s[30:31], 0, v[166:167]
	global_load_lds_dwordx4 v[178:179], off
	v_lshl_add_u64 v[178:179], v[194:195], 0, s[28:29]
	s_mov_b32 m0, s42
	s_nop 0
	global_load_lds_dwordx4 v[178:179], off
	s_waitcnt vmcnt(8)
	s_waitcnt lgkmcnt(0)
	s_barrier
	s_setprio 1
	s_waitcnt lgkmcnt(0)
	v_mfma_f32_16x16x128_f8f6f4 v[96:99], v[26:33], v[200:207], 0
	v_mfma_f32_16x16x128_f8f6f4 v[92:95], v[18:25], v[200:207], 0
	v_mfma_f32_16x16x128_f8f6f4 v[84:87], v[18:25], v[222:229], 0
	v_mfma_f32_16x16x128_f8f6f4 v[88:91], v[26:33], v[222:229], 0
	v_mfma_f32_16x16x128_f8f6f4 v[80:83], v[26:33], v[230:237], 0
	v_mfma_f32_16x16x128_f8f6f4 v[76:79], v[18:25], v[230:237], 0
	v_mfma_f32_16x16x128_f8f6f4 v[68:71], v[18:25], v[238:245], 0
	v_mfma_f32_16x16x128_f8f6f4 v[72:75], v[26:33], v[238:245], 0
	s_setprio 2
	s_setprio 1
	v_mfma_f32_16x16x128_f8f6f4 v[64:67], v[10:17], v[200:207], 0
	v_mfma_f32_16x16x128_f8f6f4 v[60:63], v[2:9], v[200:207], 0
	v_mfma_f32_16x16x128_f8f6f4 v[52:55], v[2:9], v[222:229], 0
	v_mfma_f32_16x16x128_f8f6f4 v[56:59], v[10:17], v[222:229], 0
	v_mfma_f32_16x16x128_f8f6f4 v[48:51], v[10:17], v[230:237], 0
	v_mfma_f32_16x16x128_f8f6f4 v[44:47], v[2:9], v[230:237], 0
	v_mfma_f32_16x16x128_f8f6f4 v[36:39], v[2:9], v[238:245], 0
	v_mfma_f32_16x16x128_f8f6f4 v[40:43], v[10:17], v[238:245], 0
	s_setprio 2
	s_barrier
	s_add_i32 s64, 0, 0x18000
	s_add_i32 s66, 0, 0x1c000
	v_add_u32_e32 v200, s64, v196
	v_add_u32_e32 v201, s66, v196
	ds_read_b128 v[26:29], v200
	ds_read_b128 v[30:33], v200 offset:1024
	ds_read_b128 v[18:21], v200 offset:2048
	ds_read_b128 v[22:25], v200 offset:3072
	ds_read_b128 v[10:13], v201
	ds_read_b128 v[14:17], v201 offset:1024
	ds_read_b128 v[2:5], v201 offset:2048
	ds_read_b128 v[6:9], v201 offset:3072
	s_add_u32 s36, s30, 0x20100
	s_addc_u32 s37, s31, 0
	s_mov_b32 m0, s43
	v_lshl_add_u64 v[178:179], s[36:37], 0, v[168:169]
	ds_read_b128 v[202:205], v197 offset:32768
	ds_read_b128 v[206:209], v197 offset:33792
	ds_read_b128 v[222:225], v197 offset:34816
	ds_read_b128 v[226:229], v197 offset:35840
	ds_read_b128 v[230:233], v197 offset:36864
	ds_read_b128 v[234:237], v197 offset:37888
	ds_read_b128 v[238:241], v197 offset:38912
	ds_read_b128 v[242:245], v197 offset:39936
	global_load_lds_dwordx4 v[178:179], off
	v_lshl_add_u64 v[178:179], s[36:37], 0, v[166:167]
	s_mov_b32 m0, s44
	s_nop 0
	global_load_lds_dwordx4 v[178:179], off
	s_waitcnt vmcnt(8)
	s_waitcnt lgkmcnt(0)
	s_barrier
	s_setprio 1
	s_waitcnt lgkmcnt(0)
	v_mfma_f32_16x16x128_f8f6f4 v[160:163], v[26:33], v[202:209], v[160:163]
	v_mfma_f32_16x16x128_f8f6f4 v[156:159], v[18:25], v[202:209], v[156:159]
	v_mfma_f32_16x16x128_f8f6f4 v[148:151], v[18:25], v[222:229], v[148:151]
	v_mfma_f32_16x16x128_f8f6f4 v[152:155], v[26:33], v[222:229], v[152:155]
	v_mfma_f32_16x16x128_f8f6f4 v[144:147], v[26:33], v[230:237], v[144:147]
	v_mfma_f32_16x16x128_f8f6f4 v[140:143], v[18:25], v[230:237], v[140:143]
	v_mfma_f32_16x16x128_f8f6f4 v[132:135], v[18:25], v[238:245], v[132:135]
	v_mfma_f32_16x16x128_f8f6f4 v[136:139], v[26:33], v[238:245], v[136:139]
	s_setprio 2
	s_setprio 1
	v_mfma_f32_16x16x128_f8f6f4 v[128:131], v[10:17], v[202:209], v[128:131]
	v_mfma_f32_16x16x128_f8f6f4 v[124:127], v[2:9], v[202:209], v[124:127]
	v_mfma_f32_16x16x128_f8f6f4 v[116:119], v[2:9], v[222:229], v[116:119]
	v_mfma_f32_16x16x128_f8f6f4 v[120:123], v[10:17], v[222:229], v[120:123]
	v_mfma_f32_16x16x128_f8f6f4 v[112:115], v[10:17], v[230:237], v[112:115]
	v_mfma_f32_16x16x128_f8f6f4 v[108:111], v[2:9], v[230:237], v[108:111]
	v_mfma_f32_16x16x128_f8f6f4 v[100:103], v[2:9], v[238:245], v[100:103]
	v_mfma_f32_16x16x128_f8f6f4 v[104:107], v[10:17], v[238:245], v[104:107]
	s_setprio 2
	s_barrier
	s_add_i32 s64, s64, s40
	s_mov_b64 s[24:25], 0x180
	s_add_i32 s65, s64, 0x2000
	v_lshl_add_u64 v[174:175], v[174:175], 0, s[24:25]
	s_mov_b32 m0, s64
	s_add_u32 s36, s22, 0x20180
	ds_read_b128 v[202:205], v197 offset:49152
	ds_read_b128 v[206:209], v197 offset:50176
	ds_read_b128 v[222:225], v197 offset:51200
	ds_read_b128 v[226:229], v197 offset:52224
	ds_read_b128 v[230:233], v197 offset:53248
	ds_read_b128 v[234:237], v197 offset:54272
	ds_read_b128 v[238:241], v197 offset:55296
	ds_read_b128 v[242:245], v197 offset:56320
	global_load_lds_dwordx4 v[174:175], off
	v_lshl_add_u64 v[174:175], v[190:191], 0, s[24:25]
	s_mov_b32 m0, s65
	s_addc_u32 s37, s23, 0
	s_add_i32 s66, s66, s40
	global_load_lds_dwordx4 v[174:175], off
	v_lshl_add_u64 v[174:175], s[36:37], 0, v[34:35]
	s_mov_b32 m0, s66
	s_add_i32 s67, s66, 0x2000
	global_load_lds_dwordx4 v[174:175], off
	v_lshl_add_u64 v[174:175], s[36:37], 0, v[164:165]
	s_mov_b32 m0, s67
	s_nop 0
	global_load_lds_dwordx4 v[174:175], off
	v_lshl_add_u64 v[174:175], v[192:193], 0, s[24:25]
	s_mov_b32 m0, s47
	s_nop 0
	global_load_lds_dwordx4 v[174:175], off
	v_lshl_add_u64 v[174:175], v[194:195], 0, s[24:25]
	s_mov_b32 m0, s48
	s_nop 0
	global_load_lds_dwordx4 v[174:175], off
	s_waitcnt vmcnt(8)
	s_waitcnt lgkmcnt(0)
	s_barrier
	s_setprio 1
	s_waitcnt lgkmcnt(0)
	v_mfma_f32_16x16x128_f8f6f4 v[96:99], v[26:33], v[202:209], v[96:99]
	v_mfma_f32_16x16x128_f8f6f4 v[92:95], v[18:25], v[202:209], v[92:95]
	v_mfma_f32_16x16x128_f8f6f4 v[84:87], v[18:25], v[222:229], v[84:87]
	v_mfma_f32_16x16x128_f8f6f4 v[88:91], v[26:33], v[222:229], v[88:91]
	v_mfma_f32_16x16x128_f8f6f4 v[80:83], v[26:33], v[230:237], v[80:83]
	v_mfma_f32_16x16x128_f8f6f4 v[76:79], v[18:25], v[230:237], v[76:79]
	v_mfma_f32_16x16x128_f8f6f4 v[68:71], v[18:25], v[238:245], v[68:71]
	v_mfma_f32_16x16x128_f8f6f4 v[72:75], v[26:33], v[238:245], v[72:75]
	s_setprio 2
	s_setprio 1
	v_mfma_f32_16x16x128_f8f6f4 v[64:67], v[10:17], v[202:209], v[64:67]
	v_mfma_f32_16x16x128_f8f6f4 v[60:63], v[2:9], v[202:209], v[60:63]
	v_mfma_f32_16x16x128_f8f6f4 v[52:55], v[2:9], v[222:229], v[52:55]
	v_mfma_f32_16x16x128_f8f6f4 v[56:59], v[10:17], v[222:229], v[56:59]
	v_mfma_f32_16x16x128_f8f6f4 v[48:51], v[10:17], v[230:237], v[48:51]
	v_mfma_f32_16x16x128_f8f6f4 v[44:47], v[2:9], v[230:237], v[44:47]
	v_mfma_f32_16x16x128_f8f6f4 v[36:39], v[2:9], v[238:245], v[36:39]
	v_mfma_f32_16x16x128_f8f6f4 v[40:43], v[10:17], v[238:245], v[40:43]
	s_setprio 2
	s_barrier
	s_add_u32 s30, s30, 0x20180
	s_addc_u32 s31, s31, 0
	s_add_u32 s68, s22, 0x200
	s_addc_u32 s69, s23, 0
	s_mov_b32 s70, 0
	.p2align	6
